# rebalanced expert-tile conversion (rank-phase idle WGs take 16 tiles, attention-phase converters 12 fewer), rope-Q fragments loaded together in attention prologue, pipelined wout epilogue, dn gate pre
# baseline (speedup 1.0000x reference)
; DEVI int opaque_tid() { int t = threadIdx.x; asm volatile("" : "+v"(t)); return t; }
; DEVI int v_st(int k, int c) { const int kk = (k & ~0xC) | ((k & 4) << 1) | ((k & 8) >> 1); return ((kk >> 3) * 4 + (c >> 5)) * 512 + ((kk & 7) * 32 + (c & 31)) * 2; }
; DEVI int v_rd_base(int lane) { return ((lane & 3) << 3) | (((lane >> 2) & 3) << 6) | (((lane >> 4) & 1) << 5) | (((lane >> 5) & 1) << 8); }
; #define SWRITE(b) do { *(bf16x8*)(V_lds + (b) * SHM_V + vst0) = sv0; *(bf16x8*)(V_lds + (b) * SHM_V + vst1) = sv1; \
;     *(bf16x8*)(K_lds + (b) * SHM_K + kst0) = sk0; *(bf16x8*)(K_lds + (b) * SHM_K + kst1) = sk1; *(bf16x8*)(K_lds + (b) * SHM_K + kst2) = sk2; } while (0)
; DEVI void attn_body(const bf16_t* __restrict__ Qb, const bf16_t* __restrict__ Kh, const bf16_t* __restrict__ Vh, bf16_t* __restrict__ Ob, int seq, char* lds) {
;     const int tid = opaque_tid(), wid = tid >> 6, lane = tid & 63, r32 = lane & 31, hi = lane >> 5;
;     char* V_lds = lds; char* K_lds = lds + 2 * SHM_V;
;     float* wsf = (float*)(lds + 2 * SHM_V + 2 * SHM_K) + wid * 64; float* li_l = wsf; float* al_l = wsf + 32;
;     float m_reg = -1e30f, l_reg = 0;
;     f32x16 o[4];
; #pragma unroll
;     for (int d = 0; d < 4; ++d) o[d] = (f32x16){0.f, 0.f, 0.f, 0.f, 0.f, 0.f, 0.f, 0.f, 0.f, 0.f, 0.f, 0.f, 0.f, 0.f, 0.f, 0.f};
;     bf16x8 qr[8];
;     const bf16_t* Qw = Qb + (size_t)(wid * QBLK + r32) * DQ + hi * 8;
;     char* qL = lds + 2 * SHM_V + 2 * SHM_K + NW * 64 * 4 + wid * 4096 + lane * 16;
; #pragma unroll
;     for (int d0 = 0; d0 < 8; ++d0) qr[d0] = *(const bf16x8*)(Qw + d0 * 16);
; #pragma unroll
;     for (int d0 = 8; d0 < 12; ++d0) *(bf16x8*)(qL + (d0 - 8) * 1024) = *(const bf16x8*)(Qw + d0 * 16);
;     const int sr = tid >> 4, sc = (tid & 15) * 8, vst0 = v_st(sr, sc), vst1 = v_st(32 + sr, sc);
;     const int kr0 = tid / 24, kc0 = (tid % 24) * 8, kr1 = (tid + 512) / 24, kc1 = ((tid + 512) % 24) * 8, kr2 = (tid + 1024) / 24, kc2 = ((tid + 1024) % 24) * 8;
;     const int kst0 = KSWZ(kr0, kc0 * 2), kst1 = KSWZ(kr1, kc1 * 2), kst2 = KSWZ(kr2, kc2 * 2);
;     const int vb0 = (int)(uintptr_t)V_lds + v_rd_base(lane);
;     bf16x8 sv0, sv1, sk0, sk1, sk2;
;     ...
;     f32x16 pA0, pA1, pB0, pB1; float mnA, mnB, alA, alB; bf16x8 pa0, pa1, pa2, pa3; const int NT = seq / KVBLK;
;     SLOAD(0); SWRITE(0); __syncthreads();
.LBB0_660:
	s_and_b64 vcc, exec, s[16:17]
	s_cbranch_vccz .LBB0_626
	s_ashr_i32 s42, s45, 3
	s_lshl_b32 s6, s45, 8
	s_mul_i32 s5, s42, 0x900
	s_and_b32 s43, s6, 0x700
	s_mul_hi_i32 s4, s42, 0x900
	s_add_u32 s5, s5, s43
	s_addc_u32 s4, s4, 0
	s_mulk_i32 s4, 0x180
	s_mul_hi_u32 s6, s5, 0x180
	s_add_i32 s6, s6, s4
	s_mulk_i32 s5, 0x180
	s_add_u32 s4, s12, s5
	s_addc_u32 s5, s13, s6
	s_add_u32 s4, s4, 0x18000
	s_addc_u32 s5, s5, 0
	s_mul_i32 s7, s42, 0xd8000
	v_readlane_b32 s16, v253, 60
	v_mov_b32_e32 v86, v0
	s_mul_hi_i32 s6, s42, 0xd8000
	v_readlane_b32 s17, v253, 61
	s_add_u32 s16, s16, s7
	s_addc_u32 s17, s17, s6
	v_ashrrev_i32_e32 v6, 6, v86
	s_mul_i32 s7, s42, 0x90000
	v_readlane_b32 s18, v253, 62
	v_and_b32_e32 v178, 31, v86
	v_lshlrev_b32_e32 v160, 5, v6
	s_mul_hi_i32 s6, s42, 0x90000
	v_readlane_b32 s19, v253, 63
	s_add_u32 s28, s18, s7
	v_or_b32_e32 v2, v160, v178
	v_mov_b64_e32 v[4:5], s[4:5]
	s_addc_u32 s29, s19, s6
	v_and_b32_e32 v1, 0x3fffffc0, v86
	s_add_i32 s6, 0, 0x14800
	v_bfe_u32 v179, v86, 5, 1
	v_mad_i64_i32 v[4:5], s[4:5], v2, s85, v[4:5]
	v_lshl_add_u32 v161, v1, 2, s6
	v_and_b32_e32 v1, 63, v86
	v_lshlrev_b32_e32 v2, 4, v179
	s_add_i32 s4, 0, 0x15000
	v_lshl_add_u64 v[8:9], v[4:5], 0, v[2:3]
	v_lshlrev_b32_e32 v10, 4, v1
	v_lshl_add_u32 v4, v6, 12, s4
	global_load_dwordx4 v[128:131], v[8:9], off
	global_load_dwordx4 v[124:127], v[8:9], off offset:32
	global_load_dwordx4 v[120:123], v[8:9], off offset:64
	global_load_dwordx4 v[116:119], v[8:9], off offset:96
	global_load_dwordx4 v[112:115], v[8:9], off offset:128
	global_load_dwordx4 v[108:111], v[8:9], off offset:160
	global_load_dwordx4 v[104:107], v[8:9], off offset:192
	global_load_dwordx4 v[100:103], v[8:9], off offset:224
	v_add_u32_e32 v181, v4, v10
	global_load_dwordx4 v[4:7], v[8:9], off offset:256
	global_load_dwordx4 v[12:15], v[8:9], off offset:288
	global_load_dwordx4 v[16:19], v[8:9], off offset:320
	global_load_dwordx4 v[20:23], v[8:9], off offset:352
	s_mov_b32 s4, 0x2aaaaaab
	s_movk_i32 s7, 0x190
	v_mov_b64_e32 v[68:69], s[16:17]
	s_cmp_lg_u32 0, -1
	s_cselect_b32 s6, 0, 0
	s_mov_b32 s52, s53
	s_mov_b32 s54, s53
	s_mov_b32 s55, s53
	s_mov_b32 s56, s53
	s_mov_b32 s57, s53
	s_mov_b32 s58, s53
	s_mov_b32 s59, s53
	s_mov_b32 s60, s53
	s_mov_b32 s61, s53
	s_mov_b32 s62, s53
	s_mov_b32 s63, s53
	s_mov_b32 s64, s53
	s_mov_b32 s65, s53
	s_mov_b32 s66, s53
	s_mov_b32 s67, s53
	s_mov_b32 s14, -1
	v_mov_b32_e32 v182, 0
	s_waitcnt vmcnt(0)
	ds_write_b128 v181, v[4:7]
	ds_write_b128 v181, v[12:15] offset:1024
	ds_write_b128 v181, v[16:19] offset:2048
	ds_write_b128 v181, v[20:23] offset:3072
	v_ashrrev_i32_e32 v4, 4, v86
	v_and_b32_e32 v7, 0xfffff0, v4
	v_lshlrev_b32_e32 v8, 1, v4
	v_lshlrev_b32_e32 v5, 3, v86
	v_and_or_b32 v7, v8, 8, v7
	v_lshrrev_b32_e32 v8, 1, v4
	v_and_b32_e32 v9, 3, v4
	v_and_b32_e32 v6, 0x78, v5
	v_lshrrev_b32_e32 v7, 1, v7
	v_bfe_u32 v5, v5, 5, 2
	v_and_or_b32 v8, v8, 4, v9
	v_or_b32_e32 v7, v7, v5
	v_lshlrev_b32_e32 v9, 6, v8
	v_lshlrev_b32_e32 v8, 4, v86
	v_lshlrev_b32_e32 v7, 9, v7
	v_and_b32_e32 v11, 48, v8
	v_add_u32_e32 v8, 32, v4
	v_or3_b32 v24, v7, v9, v11
	v_and_b32_e32 v7, 0xfffff0, v8
	v_lshlrev_b32_e32 v12, 1, v8
	v_and_or_b32 v7, v12, 8, v7
	v_lshrrev_b32_e32 v7, 1, v7
	v_or_b32_e32 v5, v7, v5
	v_lshlrev_b32_e32 v5, 9, v5
	v_or3_b32 v25, v5, v9, v11
	v_mul_hi_i32 v5, v86, s4
	v_lshrrev_b32_e32 v7, 31, v5
	v_ashrrev_i32_e32 v5, 2, v5
	v_add_u32_e32 v60, v5, v7
	v_add_u32_e32 v7, 0x200, v86
	v_mul_hi_i32 v9, v7, s4
	v_lshrrev_b32_e32 v11, 31, v9
	v_ashrrev_i32_e32 v9, 2, v9
	v_add_u32_e32 v64, v9, v11
	v_mul_lo_u32 v9, v64, 24
	v_sub_u32_e32 v7, v7, v9
	v_add_u32_e32 v9, 0x400, v86
	v_mul_hi_i32 v11, v9, s4
	v_lshrrev_b32_e32 v13, 31, v11
	v_ashrrev_i32_e32 v11, 2, v11
	v_add_u32_e32 v70, v11, v13
	v_mul_lo_u32 v5, v60, 24
	v_mul_lo_u32 v11, v70, 24
	v_sub_u32_e32 v5, v86, v5
	v_sub_u32_e32 v9, v9, v11
	v_mul_lo_u32 v11, v60, s7
	v_lshlrev_b32_e32 v12, 3, v5
	v_lshl_add_u32 v26, v5, 4, v11
	v_mul_lo_u32 v5, v64, s7
	v_lshl_add_u32 v27, v7, 4, v5
	v_mul_lo_u32 v5, v70, s7
	v_lshlrev_b32_e32 v16, 3, v7
	v_lshlrev_b32_e32 v20, 3, v9
	v_lshl_add_u32 v28, v9, 4, v5
	v_lshlrev_b32_e32 v5, 3, v1
	v_and_b32_e32 v7, 0xc0, v10
	v_lshlrev_b32_e32 v9, 1, v86
	v_and_or_b32 v7, v5, 24, v7
	v_and_b32_e32 v9, 32, v9
	v_and_b32_e32 v5, 0x100, v5
	v_or3_b32 v87, v7, v9, v5
	v_ashrrev_i32_e32 v5, 31, v4
	v_lshlrev_b64 v[72:73], 8, v[4:5]
	v_lshl_add_u64 v[4:5], s[28:29], 0, v[72:73]
	v_lshlrev_b32_e32 v10, 1, v6
	v_mov_b32_e32 v11, v3
	v_ashrrev_i32_e32 v9, 31, v8
	v_lshl_add_u64 v[56:57], v[4:5], 0, v[10:11]
	v_lshlrev_b64 v[8:9], 8, v[8:9]
	v_ashrrev_i32_e32 v13, 31, v12
	v_ashrrev_i32_e32 v17, 31, v16
	v_ashrrev_i32_e32 v21, 31, v20
	global_load_dwordx4 v[4:7], v[56:57], off
	v_lshl_add_u64 v[8:9], s[28:29], 0, v[8:9]
	v_mad_i64_i32 v[14:15], s[4:5], v60, s85, v[68:69]
	v_lshlrev_b64 v[76:77], 1, v[12:13]
	v_mad_i64_i32 v[18:19], s[4:5], v64, s85, v[68:69]
	v_lshlrev_b64 v[80:81], 1, v[16:17]
	v_mad_i64_i32 v[22:23], s[4:5], v70, s85, v[68:69]
	v_lshlrev_b64 v[84:85], 1, v[20:21]
	v_lshl_add_u64 v[8:9], v[8:9], 0, v[10:11]
	v_lshl_add_u64 v[12:13], v[14:15], 0, v[76:77]
	v_lshl_add_u64 v[16:17], v[18:19], 0, v[80:81]
	v_lshl_add_u64 v[20:21], v[22:23], 0, v[84:85]
	global_load_dwordx4 v[8:11], v[8:9], off
	v_add_u32_e32 v185, 0, v24
	global_load_dwordx4 v[12:15], v[12:13], off
	v_add_u32_e32 v186, 0, v25
	global_load_dwordx4 v[16:19], v[16:17], off
	v_add_u32_e32 v187, 0, v26
	global_load_dwordx4 v[20:23], v[20:21], off
	v_add_u32_e32 v188, 0, v27
	v_add_u32_e32 v189, 0, v28
	v_mad_i64_i32 v[74:75], s[4:5], v60, s85, 0
	v_mad_i64_i32 v[78:79], s[4:5], v64, s85, 0
	v_mad_i64_i32 v[82:83], s[4:5], v70, s85, 0
	s_movk_i32 s4, 0x4000
	v_add_u32_e32 v60, 64, v60
	v_add_u32_e32 v64, 64, v64
	v_add_u32_e32 v70, 64, v70
	v_add_u32_e32 v180, s6, v87
	s_waitcnt vmcnt(4)
	ds_write_b128 v185, v[4:7]
	v_mad_u32_u24 v4, v178, s7, v2
	v_add_u32_e32 v184, 0, v4
	v_add_u32_e32 v88, 0x3200, v4
	v_add_u32_e32 v190, 0x3200, v184
	v_add_u32_e32 v193, 0, v88
	s_waitcnt vmcnt(3)
	ds_write_b128 v186, v[8:11]
	s_waitcnt vmcnt(2)
	ds_write_b128 v187, v[12:15] offset:32768
	s_waitcnt vmcnt(1)
	ds_write_b128 v188, v[16:19] offset:32768
	v_mov_b64_e32 v[4:5], s[52:53]
	s_waitcnt vmcnt(0)
	ds_write_b128 v189, v[20:23] offset:32768
	s_waitcnt lgkmcnt(0)
	s_barrier
; DEVI void partialSM(f32x16& p0, f32x16& p1, float& m_reg, float& mn, float& alpha) {
;     constexpr float C = 1.4426950408889634f;
;     float pmax = p0[0];
; #pragma unroll
;     for (int r = 1; r < 16; ++r) pmax = fmaxf(pmax, p0[r]);
; #pragma unroll
;     for (int r = 0; r < 16; ++r) pmax = fmaxf(pmax, p1[r]);
;     { auto rr = __builtin_amdgcn_permlane32_swap(__float_as_uint(pmax), __float_as_uint(pmax), false, false);
;       pmax = fmaxf(__uint_as_float(rr[0]), __uint_as_float(rr[1])); }
;     if (__builtin_expect(__all(pmax - m_reg <= THR), 1)) { mn = m_reg; alpha = 1.f; }
;     else { mn = fmaxf(m_reg, pmax); alpha = __builtin_amdgcn_exp2f((m_reg - mn) * C); m_reg = mn; }
;     const float mnC = -mn * C;
; #pragma unroll
;     for (int r = 0; r < 16; ++r) p0[r] = fmaf(p0[r], C, mnC);
; #pragma unroll
;     for (int r = 0; r < 16; ++r) p1[r] = fmaf(p1[r], C, mnC);
; #pragma unroll
;     for (int r = 0; r < 16; ++r) p0[r] = __builtin_amdgcn_exp2f(p0[r]);
; }
; DEVI void qkt(f32x16& p0, f32x16& p1, const char* Ks, const bf16x8* qr, const char* qL, int r32, int hi) {
;     p0 = (f32x16){0.f, 0.f, 0.f, 0.f, 0.f, 0.f, 0.f, 0.f, 0.f, 0.f, 0.f, 0.f, 0.f, 0.f, 0.f, 0.f}; p1 = p0;
; #pragma unroll
;     for (int d0 = 0; d0 < 12; ++d0) { const int cb = (d0 * 16 + hi * 8) * 2;
;         const bf16x8 b0 = *(const bf16x8*)(Ks + KSWZ(r32, cb));
;         const bf16x8 b1 = *(const bf16x8*)(Ks + KSWZ(32 + r32, cb));
;         const bf16x8 qv = (d0 < 8) ? qr[d0 < 8 ? d0 : 0] : *(const bf16x8*)(qL + (d0 - 8) * 1024);
;         p0 = __builtin_amdgcn_mfma_f32_32x32x16_bf16(b0, qv, p0, 0, 0, 0);
;         p1 = __builtin_amdgcn_mfma_f32_32x32x16_bf16(b1, qv, p1, 0, 0, 0); }
; }
	ds_read_b128 v[36:39], v184 offset:45568
	ds_read_b128 v[20:23], v184 offset:32768
	ds_read_b128 v[52:55], v184 offset:32800
	s_waitcnt lgkmcnt(1)
	v_mfma_f32_32x32x16_bf16 v[20:35], v[20:23], v[128:131], 0
	ds_read_b128 v[90:93], v184 offset:45600
	v_mov_b64_e32 v[18:19], s[66:67]
	v_mov_b64_e32 v[6:7], s[54:55]
	v_mov_b64_e32 v[8:9], s[56:57]
	v_mov_b64_e32 v[10:11], s[58:59]
	v_mov_b64_e32 v[12:13], s[60:61]
	v_mov_b64_e32 v[14:15], s[62:63]
	v_mfma_f32_32x32x16_bf16 v[36:51], v[36:39], v[128:131], 0
	v_mov_b64_e32 v[16:17], s[64:65]
	v_readlane_b32 s60, v254, 59
	v_readlane_b32 s66, v254, 51
	s_mov_b32 s65, 0x4deb6000
	s_mov_b32 s63, 0x484b6000
	s_movk_i32 s64, 0x78
	v_readlane_b32 s61, v254, 60
	s_waitcnt lgkmcnt(1)
	v_mfma_f32_32x32x16_bf16 v[20:35], v[52:55], v[124:127], v[20:35]
	v_readlane_b32 s67, v254, 52
	s_waitcnt lgkmcnt(0)
	v_mfma_f32_32x32x16_bf16 v[36:51], v[90:93], v[124:127], v[36:51]
	ds_read_b128 v[52:55], v184 offset:32832
	ds_read_b128 v[90:93], v184 offset:45632
	s_waitcnt lgkmcnt(1)
	v_mfma_f32_32x32x16_bf16 v[20:35], v[52:55], v[120:123], v[20:35]
	s_waitcnt lgkmcnt(0)
	v_mfma_f32_32x32x16_bf16 v[36:51], v[90:93], v[120:123], v[36:51]
	ds_read_b128 v[52:55], v184 offset:32864
	ds_read_b128 v[90:93], v184 offset:45664
	s_waitcnt lgkmcnt(1)
	v_mfma_f32_32x32x16_bf16 v[20:35], v[52:55], v[116:119], v[20:35]
	s_waitcnt lgkmcnt(0)
	v_mfma_f32_32x32x16_bf16 v[36:51], v[90:93], v[116:119], v[36:51]
	ds_read_b128 v[52:55], v184 offset:32896
	ds_read_b128 v[90:93], v184 offset:45696
	s_waitcnt lgkmcnt(1)
	v_mfma_f32_32x32x16_bf16 v[20:35], v[52:55], v[112:115], v[20:35]
	s_waitcnt lgkmcnt(0)
	v_mfma_f32_32x32x16_bf16 v[36:51], v[90:93], v[112:115], v[36:51]
	ds_read_b128 v[52:55], v184 offset:32928
	ds_read_b128 v[90:93], v184 offset:45728
	s_waitcnt lgkmcnt(1)
	v_mfma_f32_32x32x16_bf16 v[20:35], v[52:55], v[108:111], v[20:35]
	s_waitcnt lgkmcnt(0)
	v_mfma_f32_32x32x16_bf16 v[36:51], v[90:93], v[108:111], v[36:51]
	ds_read_b128 v[52:55], v184 offset:32960
	ds_read_b128 v[90:93], v184 offset:45760
	s_waitcnt lgkmcnt(1)
	v_mfma_f32_32x32x16_bf16 v[20:35], v[52:55], v[104:107], v[20:35]
	s_waitcnt lgkmcnt(0)
	v_mfma_f32_32x32x16_bf16 v[36:51], v[90:93], v[104:107], v[36:51]
	ds_read_b128 v[52:55], v184 offset:32992
	ds_read_b128 v[90:93], v184 offset:45792
	s_waitcnt lgkmcnt(1)
	v_mfma_f32_32x32x16_bf16 v[20:35], v[52:55], v[100:103], v[20:35]
	s_waitcnt lgkmcnt(0)
	v_mfma_f32_32x32x16_bf16 v[36:51], v[90:93], v[100:103], v[36:51]
	ds_read_b128 v[52:55], v184 offset:33024
	ds_read_b128 v[90:93], v184 offset:45824
	ds_read_b128 v[94:97], v181
	s_waitcnt lgkmcnt(0)
	v_mfma_f32_32x32x16_bf16 v[20:35], v[52:55], v[94:97], v[20:35]
	v_mfma_f32_32x32x16_bf16 v[36:51], v[90:93], v[94:97], v[36:51]
	ds_read_b128 v[52:55], v184 offset:33056
	ds_read_b128 v[90:93], v184 offset:45856
	ds_read_b128 v[94:97], v181 offset:1024
	s_waitcnt lgkmcnt(0)
	v_mfma_f32_32x32x16_bf16 v[20:35], v[52:55], v[94:97], v[20:35]
	v_mfma_f32_32x32x16_bf16 v[36:51], v[90:93], v[94:97], v[36:51]
	ds_read_b128 v[52:55], v184 offset:33088
	ds_read_b128 v[90:93], v184 offset:45888
	ds_read_b128 v[94:97], v181 offset:2048
	s_waitcnt lgkmcnt(0)
	v_mfma_f32_32x32x16_bf16 v[20:35], v[52:55], v[94:97], v[20:35]
	v_mfma_f32_32x32x16_bf16 v[36:51], v[90:93], v[94:97], v[36:51]
	ds_read_b128 v[52:55], v184 offset:33120
	ds_read_b128 v[90:93], v184 offset:45920
	ds_read_b128 v[94:97], v181 offset:3072
	s_waitcnt lgkmcnt(0)
	v_mfma_f32_32x32x16_bf16 v[20:35], v[52:55], v[94:97], v[20:35]
	v_mfma_f32_32x32x16_bf16 v[36:51], v[90:93], v[94:97], v[36:51]
	s_nop 10
	v_max_f32_e32 v52, v21, v21
	v_max_f32_e32 v53, v20, v20
	v_max_f32_e32 v52, v53, v52
	v_max3_f32 v52, v52, v22, v23
	v_max3_f32 v52, v52, v24, v25
	v_max3_f32 v52, v52, v26, v27
	v_max3_f32 v52, v52, v28, v29
	v_max3_f32 v52, v52, v30, v31
	v_max3_f32 v52, v52, v32, v33
	v_max3_f32 v52, v52, v34, v35
	v_max3_f32 v52, v52, v36, v37
	v_max3_f32 v52, v52, v38, v39
	v_max3_f32 v52, v52, v40, v41
	v_max3_f32 v52, v52, v42, v43
	v_max3_f32 v52, v52, v44, v45
	v_max3_f32 v52, v52, v46, v47
	v_max3_f32 v52, v52, v48, v49
	v_max3_f32 v52, v52, v50, v51
	v_mov_b32_e32 v53, v52
	s_nop 1
	v_permlane32_swap_b32_e32 v52, v53
	v_max_f32_e32 v53, v53, v53
	v_max_f32_e32 v52, v52, v52
	v_max_f32_e32 v89, v52, v53
	v_add_f32_e32 v52, 0x7149f2ca, v89
	v_cmp_ge_f32_e32 vcc, s3, v52
	v_add_co_u32_e64 v52, s[38:39], s4, v56
	s_movk_i32 s4, 0x6000
	s_nop 0
	v_addc_co_u32_e64 v53, s[38:39], 0, v57, s[38:39]
	v_add_co_u32_e64 v56, s[38:39], s4, v56
	global_load_dwordx4 v[52:55], v[52:53], off
	s_nop 0
	v_addc_co_u32_e64 v57, s[38:39], 0, v57, s[38:39]
	v_mad_i64_i32 v[60:61], s[4:5], v60, s85, v[68:69]
	global_load_dwordx4 v[56:59], v[56:57], off
	v_lshl_add_u64 v[60:61], v[60:61], 0, v[76:77]
	v_mad_i64_i32 v[64:65], s[4:5], v64, s85, v[68:69]
	global_load_dwordx4 v[60:63], v[60:61], off
	v_lshl_add_u64 v[64:65], v[64:65], 0, v[80:81]
	v_mad_i64_i32 v[68:69], s[4:5], v70, s85, v[68:69]
	global_load_dwordx4 v[64:67], v[64:65], off
	v_lshl_add_u64 v[68:69], v[68:69], 0, v[84:85]
	global_load_dwordx4 v[68:71], v[68:69], off
	s_cmp_eq_u64 vcc, exec
	s_waitcnt vmcnt(4)
; #define SLOAD(k0) do { sv0 = *(const bf16x8*)(Vh + (size_t)((k0) + sr) * DV + sc); sv1 = *(const bf16x8*)(Vh + (size_t)((k0) + 32 + sr) * DV + sc); \
;     sk0 = *(const bf16x8*)(Kh + (size_t)((k0) + kr0) * DQ + kc0); sk1 = *(const bf16x8*)(Kh + (size_t)((k0) + kr1) * DQ + kc1); sk2 = *(const bf16x8*)(Kh + (size_t)((k0) + kr2) * DQ + kc2); } while (0)
; #define SWRITE(b) do { *(bf16x8*)(V_lds + (b) * SHM_V + vst0) = sv0; *(bf16x8*)(V_lds + (b) * SHM_V + vst1) = sv1; \
;     *(bf16x8*)(K_lds + (b) * SHM_K + kst0) = sk0; *(bf16x8*)(K_lds + (b) * SHM_K + kst1) = sk1; *(bf16x8*)(K_lds + (b) * SHM_K + kst2) = sk2; } while (0)
; DEVI void partialSM(f32x16& p0, f32x16& p1, float& m_reg, float& mn, float& alpha) {
;     ...
;     const float mnC = -mn * C;
; #pragma unroll
;     for (int r = 0; r < 16; ++r) p0[r] = fmaf(p0[r], C, mnC);
; #pragma unroll
;     for (int r = 0; r < 16; ++r) p1[r] = fmaf(p1[r], C, mnC);
; #pragma unroll
;     for (int r = 0; r < 16; ++r) p0[r] = __builtin_amdgcn_exp2f(p0[r]);
; DEVI void attn_body(const bf16_t* __restrict__ Qb, const bf16_t* __restrict__ Kh, const bf16_t* __restrict__ Vh, bf16_t* __restrict__ Ob, int seq, char* lds) {
;     ...
;     SLOAD(0); SWRITE(0); __syncthreads();
;     qkt(pA0, pA1, K_lds, qr, qL, r32, hi); partialSM(pA0, pA1, m_reg, mnA, alA);
;     SLOAD(KVBLK); SWRITE(1); __syncthreads();
	ds_write_b128 v185, v[52:55] offset:16384
	s_waitcnt vmcnt(3)
	ds_write_b128 v186, v[56:59] offset:16384
	s_waitcnt vmcnt(2)
	ds_write_b128 v187, v[60:63] offset:58368
	s_waitcnt vmcnt(1)
	ds_write_b128 v188, v[64:67] offset:58368
	s_waitcnt vmcnt(0)
	ds_write_b128 v189, v[68:71] offset:58368
	s_cselect_b64 vcc, -1, 0
	v_max_f32_e32 v53, 0xf149f2ca, v89
	v_mov_b32_e32 v52, 0xf149f2ca
	v_cndmask_b32_e32 v191, v53, v52, vcc
	v_mul_f32_e32 v52, 0xbfb8aa3b, v191
	v_fmamk_f32 v20, v20, 0x3fb8aa3b, v52
	v_exp_f32_e32 v148, v20
	v_fmamk_f32 v20, v21, 0x3fb8aa3b, v52
	v_exp_f32_e32 v172, v20
	v_fmamk_f32 v20, v22, 0x3fb8aa3b, v52
	v_exp_f32_e32 v149, v20
	v_fmamk_f32 v20, v23, 0x3fb8aa3b, v52
	v_exp_f32_e32 v173, v20
	v_fmamk_f32 v20, v24, 0x3fb8aa3b, v52
	v_exp_f32_e32 v150, v20
	v_fmamk_f32 v20, v25, 0x3fb8aa3b, v52
	v_exp_f32_e32 v174, v20
	v_fmamk_f32 v20, v26, 0x3fb8aa3b, v52
	v_exp_f32_e32 v151, v20
	v_fmamk_f32 v20, v27, 0x3fb8aa3b, v52
	v_exp_f32_e32 v171, v20
	v_fmamk_f32 v20, v28, 0x3fb8aa3b, v52
	v_exp_f32_e32 v156, v20
	v_fmamk_f32 v20, v29, 0x3fb8aa3b, v52
	v_exp_f32_e32 v158, v20
	v_fmamk_f32 v20, v30, 0x3fb8aa3b, v52
	v_exp_f32_e32 v157, v20
	v_fmamk_f32 v20, v31, 0x3fb8aa3b, v52
	v_exp_f32_e32 v170, v20
	v_fmamk_f32 v20, v32, 0x3fb8aa3b, v52
	v_exp_f32_e32 v153, v20
	v_fmamk_f32 v20, v33, 0x3fb8aa3b, v52
	v_pk_fma_f32 v[144:145], v[36:37], s[72:73], v[52:53] op_sel_hi:[1,0,0]
	v_sub_f32_e32 v36, 0xf149f2ca, v53
	v_exp_f32_e32 v155, v20
	v_fmamk_f32 v20, v34, 0x3fb8aa3b, v52
	v_mul_f32_e32 v36, 0x3fb8aa3b, v36
	v_exp_f32_e32 v154, v20
	v_mad_i64_i32 v[20:21], s[4:5], s42, v222, v[82:83]
	v_exp_f32_e32 v36, v36
	v_lshl_add_u64 v[162:163], v[20:21], 0, v[84:85]
	v_mad_i64_i32 v[20:21], s[4:5], s42, v222, v[78:79]
	v_lshl_add_u64 v[164:165], v[20:21], 0, v[80:81]
	v_mad_i64_i32 v[20:21], s[4:5], s42, v222, v[74:75]
	v_lshl_add_u64 v[166:167], v[20:21], 0, v[76:77]
	v_mov_b32_e32 v20, 0x90000
	v_pk_fma_f32 v[132:133], v[50:51], s[72:73], v[52:53] op_sel_hi:[1,0,0]
	v_pk_fma_f32 v[138:139], v[48:49], s[72:73], v[52:53] op_sel_hi:[1,0,0]
	v_pk_fma_f32 v[146:147], v[46:47], s[72:73], v[52:53] op_sel_hi:[1,0,0]
	v_pk_fma_f32 v[134:135], v[44:45], s[72:73], v[52:53] op_sel_hi:[1,0,0]
	v_pk_fma_f32 v[136:137], v[42:43], s[72:73], v[52:53] op_sel_hi:[1,0,0]
	v_pk_fma_f32 v[140:141], v[40:41], s[72:73], v[52:53] op_sel_hi:[1,0,0]
	v_pk_fma_f32 v[142:143], v[38:39], s[72:73], v[52:53] op_sel_hi:[1,0,0]
	v_fmac_f32_e32 v52, 0x3fb8aa3b, v35
	v_mad_i64_i32 v[168:169], s[4:5], s42, v20, v[72:73]
	v_and_b32_e32 v20, 15, v86
	v_cndmask_b32_e64 v192, v36, 1.0, vcc
	v_exp_f32_e32 v159, v52
	s_addk_i32 s6, 0x4000
	v_lshl_or_b32 v168, v20, 4, v168
	v_mov_b64_e32 v[66:67], v[18:19]
	v_mov_b64_e32 v[50:51], v[18:19]
	v_mov_b64_e32 v[34:35], v[18:19]
	s_waitcnt lgkmcnt(0)
	s_barrier
	v_cmp_gt_u32_e64 s[38:39], 32, v1
	v_lshl_add_u32 v1, v178, 2, v161
	v_add_u32_e32 v183, s6, v87
	v_mov_b64_e32 v[64:65], v[16:17]
	v_mov_b64_e32 v[62:63], v[14:15]
	v_mov_b64_e32 v[60:61], v[12:13]
	v_mov_b64_e32 v[58:59], v[10:11]
	v_mov_b64_e32 v[56:57], v[8:9]
	v_mov_b64_e32 v[54:55], v[6:7]
	v_mov_b64_e32 v[52:53], v[4:5]
	v_mov_b64_e32 v[48:49], v[16:17]
	v_mov_b64_e32 v[46:47], v[14:15]
	v_mov_b64_e32 v[44:45], v[12:13]
	v_mov_b64_e32 v[42:43], v[10:11]
	v_mov_b64_e32 v[40:41], v[8:9]
	v_mov_b64_e32 v[38:39], v[6:7]
	v_mov_b64_e32 v[36:37], v[4:5]
	v_mov_b64_e32 v[32:33], v[16:17]
	v_mov_b64_e32 v[30:31], v[14:15]
	v_mov_b64_e32 v[28:29], v[12:13]
	v_mov_b64_e32 v[26:27], v[10:11]
	v_mov_b64_e32 v[24:25], v[8:9]
	v_mov_b64_e32 v[22:23], v[6:7]
	v_mov_b64_e32 v[20:21], v[4:5]

; DEVI int opaque_tid() { int t = threadIdx.x; asm volatile("" : "+v"(t)); return t; }
; DEVI void cvt8_load(const Params& p, int L, int t, CvtIn& in) {
;     const int which = t / 4096, r = t % 4096, le = L * 16 + r / 256, kt = (r % 256) / 16, nt = r % 16;
;     const float* src = (which == 2 ? p.w_down : (which == 0 ? p.w_gate : p.w_up)) + (size_t)le * 2048 * 2048;
;     const int tid = opaque_tid(), nq = tid & 31, kq0 = tid >> 5;
; #pragma unroll
;     for (int it = 0; it < 2; ++it)
; #pragma unroll
;         for (int kk = 0; kk < 4; ++kk) in.v[it * 4 + kk] = __builtin_nontemporal_load((const f32x4*)(src + (size_t)(kt * 128 + (kq0 + it * 16) * 4 + kk) * 2048 + nt * 128 + nq * 4));
; }
; DEVI void cvt8_stream3(const Params& p, int L, int t0, int step, int count, char* smem) {
;     if (count <= 0) return;
;     CvtIn a, b; cvt8_load(p, L, t0, a);
;     if (count > 1) cvt8_load(p, L, t0 + step, b);
.LBB0_773:
	s_and_b64 vcc, exec, s[16:17]
	s_cbranch_vccz .LBB0_801
	v_readlane_b32 s4, v255, 0
	v_readlane_b32 s5, v255, 1
	s_mov_b32 s6, s2
	s_mov_b64 s[16:17], -1
	s_and_b64 vcc, exec, s[4:5]
	s_cbranch_vccz .LBB0_784
	s_add_i32 s7, s6, 0x1cd0
	s_and_b32 s4, s7, 0xfffff000
	s_add_i32 s5, s6, 0x2ccf
	s_cmpk_lt_u32 s5, 0x1fff
	s_cselect_b32 s5, s64, 0x80
	s_cmpk_lg_i32 s4, 0x2000
	s_cselect_b32 s4, s5, 0x88
	s_add_u32 s4, s0, s4
	s_addc_u32 s5, s1, 0
	s_ashr_i32 s14, s7, 31
	s_lshr_b32 s14, s14, 20
	s_add_i32 s14, s7, s14
	s_and_b32 s14, s14, 0xf000
	s_sub_i32 s7, s7, s14
	s_sext_i32_i16 s14, s7
	s_lshr_b32 s14, s14, 15
	s_bfe_u32 s16, s14, 0x4000c
	s_add_i32 s16, s7, s16
	s_and_b32 s16, s16, 0xfff0
	s_bfe_u32 s14, s14, 0x80008
	s_sub_i32 s16, s7, s16
	s_add_i32 s14, s7, s14
	s_sext_i32_i16 s18, s16
	s_sext_i32_i16 s16, s14
	s_and_b32 s14, s14, 0xff00
	s_load_dwordx2 s[4:5], s[4:5], 0x0
	s_ashr_i32 s16, s16, 8
	s_sub_i32 s7, s7, s14
	s_sext_i32_i16 s14, s7
	s_add_i32 s16, s16, 16
	s_bfe_u32 s14, s14, 0x4001b
	s_and_b32 s52, s16, 0xffff
	s_add_i32 s7, s7, s14
	s_lshl_b64 s[16:17], s[52:53], 24
	s_sext_i32_i16 s7, s7
	s_waitcnt lgkmcnt(0)
	s_add_u32 s14, s4, s16
	v_mov_b32_e32 v1, v0
	s_addc_u32 s16, s5, s17
	s_lshl_b32 s4, s7, 3
	v_ashrrev_i32_e32 v2, 3, v1
	s_and_b32 s4, s4, 0xffffff80
	v_and_b32_e32 v2, -4, v2
	s_waitcnt vmcnt(2)
	v_add_u32_e32 v4, s4, v2
	s_lshl_b32 s4, s18, 7
	s_ashr_i32 s5, s4, 31
	s_lshl_b64 s[4:5], s[4:5], 2
	s_add_u32 s4, s14, s4
	v_lshlrev_b32_e32 v1, 4, v1
	s_addc_u32 s5, s16, s5
	v_and_b32_e32 v2, 0x1f0, v1
	v_ashrrev_i32_e32 v5, 31, v4
	v_lshl_add_u64 v[6:7], s[4:5], 0, v[2:3]
	s_waitcnt vmcnt(1)
	v_lshlrev_b64 v[8:9], 13, v[4:5]
	v_lshl_add_u64 v[12:13], v[6:7], 0, v[8:9]
	v_or_b32_e32 v8, 1, v4
	v_ashrrev_i32_e32 v9, 31, v8
	v_lshlrev_b64 v[8:9], 13, v[8:9]
	v_lshl_add_u64 v[8:9], v[6:7], 0, v[8:9]
	global_load_dwordx4 v[20:23], v[12:13], off nt
	global_load_dwordx4 v[24:27], v[8:9], off nt
	v_or_b32_e32 v8, 2, v4
	v_or_b32_e32 v4, 3, v4
	v_ashrrev_i32_e32 v9, 31, v8
	v_ashrrev_i32_e32 v5, 31, v4
	v_lshlrev_b64 v[8:9], 13, v[8:9]
	v_lshlrev_b64 v[4:5], 13, v[4:5]
	v_lshl_add_u64 v[8:9], v[6:7], 0, v[8:9]
	v_lshl_add_u64 v[4:5], v[6:7], 0, v[4:5]
	global_load_dwordx4 v[28:31], v[8:9], off nt
	global_load_dwordx4 v[32:35], v[4:5], off nt
	v_add_co_u32_e32 v4, vcc, s94, v12
	s_mov_b32 s19, 0x82000
	s_nop 0
	v_addc_co_u32_e32 v5, vcc, 0, v13, vcc
	v_add_co_u32_e32 v8, vcc, s19, v12
	s_mov_b32 s4, 0x84000
	s_nop 0
	v_addc_co_u32_e32 v9, vcc, 0, v13, vcc
	v_add_co_u32_e32 v14, vcc, s4, v12
	s_mov_b32 s4, 0x86000
	s_nop 0
	v_addc_co_u32_e32 v15, vcc, 0, v13, vcc
	s_add_i32 s7, s6, 0x1cf0
	v_add_co_u32_e32 v16, vcc, s4, v12
	s_and_b32 s4, s7, 0xfffff000
	s_add_i32 s5, s6, 0x2cef
	s_cmpk_lt_u32 s5, 0x1fff
	s_cselect_b32 s5, s64, 0x80
	s_cmpk_lg_i32 s4, 0x2000
	s_cselect_b32 s4, s5, 0x88
	s_add_u32 s4, s0, s4
	s_addc_u32 s5, s1, 0
	s_ashr_i32 s14, s7, 31
	s_lshr_b32 s14, s14, 20
	s_add_i32 s14, s7, s14
	s_and_b32 s14, s14, 0xf000
	s_sub_i32 s7, s7, s14
	s_sext_i32_i16 s14, s7
	s_lshr_b32 s14, s14, 15
	s_bfe_u32 s16, s14, 0x4000c
	s_add_i32 s16, s7, s16
	s_and_b32 s16, s16, 0xfff0
	s_bfe_u32 s14, s14, 0x80008
	v_addc_co_u32_e32 v17, vcc, 0, v13, vcc
	s_sub_i32 s16, s7, s16
	s_add_i32 s14, s7, s14
	global_load_dwordx4 v[4:7], v[4:5], off nt
	s_nop 0
	global_load_dwordx4 v[8:11], v[8:9], off nt
	s_nop 0
	global_load_dwordx4 v[12:15], v[14:15], off nt
	s_nop 0
	global_load_dwordx4 v[16:19], v[16:17], off nt
	s_sext_i32_i16 s18, s16
	s_sext_i32_i16 s16, s14
	s_and_b32 s14, s14, 0xff00
	s_load_dwordx2 s[4:5], s[4:5], 0x0
	s_ashr_i32 s16, s16, 8
	s_sub_i32 s7, s7, s14
	s_sext_i32_i16 s14, s7
	s_add_i32 s16, s16, 16
	s_bfe_u32 s14, s14, 0x4001b
	s_and_b32 s52, s16, 0xffff
	s_add_i32 s7, s7, s14
	s_lshl_b64 s[16:17], s[52:53], 24
	s_sext_i32_i16 s7, s7
	s_waitcnt lgkmcnt(0)
	s_add_u32 s14, s4, s16
	v_mov_b32_e32 v1, v0
	s_addc_u32 s16, s5, s17
	s_lshl_b32 s4, s7, 3
	v_ashrrev_i32_e32 v2, 3, v1
	s_and_b32 s4, s4, 0xffffff80
	v_and_b32_e32 v2, -4, v2
	v_add_u32_e32 v44, s4, v2
	s_lshl_b32 s4, s18, 7
	s_ashr_i32 s5, s4, 31
	s_lshl_b64 s[4:5], s[4:5], 2
	s_add_u32 s4, s14, s4
	v_lshlrev_b32_e32 v1, 4, v1
	s_addc_u32 s5, s16, s5
	v_and_b32_e32 v2, 0x1f0, v1
	v_ashrrev_i32_e32 v45, 31, v44
	v_lshl_add_u64 v[46:47], s[4:5], 0, v[2:3]
	v_lshlrev_b64 v[36:37], 13, v[44:45]
	v_lshl_add_u64 v[48:49], v[46:47], 0, v[36:37]
	v_or_b32_e32 v36, 1, v44
	v_or_b32_e32 v50, 2, v44
	v_or_b32_e32 v44, 3, v44
	v_ashrrev_i32_e32 v37, 31, v36
	v_ashrrev_i32_e32 v51, 31, v50
	v_ashrrev_i32_e32 v45, 31, v44
	v_lshlrev_b64 v[36:37], 13, v[36:37]
	v_lshlrev_b64 v[50:51], 13, v[50:51]
	v_lshlrev_b64 v[44:45], 13, v[44:45]
	v_lshl_add_u64 v[40:41], v[46:47], 0, v[36:37]
	v_lshl_add_u64 v[50:51], v[46:47], 0, v[50:51]
	v_lshl_add_u64 v[44:45], v[46:47], 0, v[44:45]
	global_load_dwordx4 v[36:39], v[48:49], off nt
	s_nop 0
	global_load_dwordx4 v[40:43], v[40:41], off nt
	s_nop 0
	global_load_dwordx4 v[72:75], v[50:51], off nt
	global_load_dwordx4 v[76:79], v[44:45], off nt
	v_add_co_u32_e32 v44, vcc, s94, v48
	s_mov_b32 s4, 0
	s_nop 0
	v_addc_co_u32_e32 v45, vcc, 0, v49, vcc
	v_add_co_u32_e32 v46, vcc, s19, v48
	s_add_i32 s5, s6, 0x2d0f
	s_nop 0
	v_addc_co_u32_e32 v47, vcc, 0, v49, vcc
	global_load_dwordx4 v[84:87], v[44:45], off nt
	global_load_dwordx4 v[88:91], v[46:47], off nt
	v_add_co_u32_e32 v44, vcc, 0x84000, v48
	s_nop 1
	v_addc_co_u32_e32 v45, vcc, 0, v49, vcc
	v_add_co_u32_e32 v46, vcc, 0x86000, v48
	s_nop 1
	v_addc_co_u32_e32 v47, vcc, 0, v49, vcc
	global_load_dwordx4 v[92:95], v[44:45], off nt
	global_load_dwordx4 v[96:99], v[46:47], off nt
	s_branch .LBB0_777
; DEVI int opaque_tid() { int t = threadIdx.x; asm volatile("" : "+v"(t)); return t; }
; DEVI unsigned cvt4_fp8(float a, float b, float c, float d) { int w = 0; w = __builtin_amdgcn_cvt_pk_fp8_f32(a, b, w, false); w = __builtin_amdgcn_cvt_pk_fp8_f32(c, d, w, true); return (unsigned)w; }
; DEVI void cvt8_finish(const Params& p, int L, int t, const CvtIn& in, char* smem) {
;     const int which = t / 4096, r = t % 4096, le = L * 16 + r / 256, kt = (r % 256) / 16, nt = r % 16;
;     unsigned char* dst = (which == 2) ? (unsigned char*)(p.ws + WS_WDN) + (size_t)le * 2048 * 2048 + (size_t)(nt * 128) * 2048
;                                       : (unsigned char*)(p.ws + WS_WGU) + (size_t)le * 4096 * 2048 + (size_t)(nt * 256 + which * 128) * 2048;
;     unsigned char* T = (unsigned char*)smem;
;     const int tid = opaque_tid(), nq = tid & 31, kq0 = tid >> 5;
; #pragma unroll
;     for (int it = 0; it < 2; ++it) { const int kq = kq0 + it * 16;
; #pragma unroll
;         for (int j = 0; j < 4; ++j) *(unsigned*)(T + (nq * 4 + j) * 144 + kq * 4) =
;             cvt4_fp8(in.v[it * 4][j] * W8_SCALE, in.v[it * 4 + 1][j] * W8_SCALE, in.v[it * 4 + 2][j] * W8_SCALE, in.v[it * 4 + 3][j] * W8_SCALE); }
;     __syncthreads();
; #pragma unroll
;     for (int i = 0; i < 2; ++i) { const int nl = (tid >> 3) + 64 * i, kc = (tid & 7) * 16;
;         *(u32x4*)(dst + (size_t)nl * 2048 + kt * 128 + kc) = *(const u32x4*)(T + nl * 144 + kc); }
;     __syncthreads();
; }
; DEVI void cvt8_stream3(const Params& p, int L, int t0, int step, int count, char* smem) {
;     ...
;     for (int i = 0; i < count; ++i) { CvtIn c;
;         if (i + 2 < count) cvt8_load(p, L, t0 + (i + 2) * step, c);
;         cvt8_finish(p, L, t0 + i * step, a, smem);
;         a = b; b = c; }
.LBB0_776:
	v_mul_f32_e32 v20, 0x42800000, v20
	v_mul_f32_e32 v24, 0x42800000, v24
	v_mov_b32_e32 v101, v3
	v_cvt_pk_fp8_f32 v101, v20, v24
	v_mul_f32_e32 v24, 0x42800000, v28
	v_mul_f32_e32 v28, 0x42800000, v32
	v_mov_b32_e32 v1, v0
	v_cvt_pk_fp8_f32 v101, v24, v28 op_sel:[0,0,1]
	v_mul_f32_e32 v21, 0x42800000, v21
	v_mul_f32_e32 v24, 0x42800000, v25
	v_mov_b32_e32 v25, v3
	v_cvt_pk_fp8_f32 v25, v21, v24
	v_lshlrev_b32_e32 v2, 2, v1
	v_and_b32_e32 v2, 0x7c, v2
	v_ashrrev_i32_e32 v100, 3, v1
	v_and_b32_e32 v20, -4, v100
	v_mul_u32_u24_e32 v2, 0x90, v2
	v_add3_u32 v2, 0, v20, v2
	v_mul_f32_e32 v20, 0x42800000, v29
	v_mul_f32_e32 v21, 0x42800000, v33
	v_cvt_pk_fp8_f32 v25, v20, v21 op_sel:[0,0,1]
	v_mul_f32_e32 v20, 0x42800000, v22
	v_mul_f32_e32 v21, 0x42800000, v26
	v_mov_b32_e32 v26, v3
	v_cvt_pk_fp8_f32 v26, v20, v21
	v_mul_f32_e32 v20, 0x42800000, v23
	v_mul_f32_e32 v21, 0x42800000, v27
	v_mov_b32_e32 v23, v3
	v_cvt_pk_fp8_f32 v23, v20, v21
	v_mul_f32_e32 v20, 0x42800000, v31
	v_mul_f32_e32 v21, 0x42800000, v35
	v_mul_f32_e32 v4, 0x42800000, v4
	v_cvt_pk_fp8_f32 v23, v20, v21 op_sel:[0,0,1]
	v_mul_f32_e32 v8, 0x42800000, v8
	v_mov_b32_e32 v20, v3
	v_cvt_pk_fp8_f32 v20, v4, v8
	v_mul_f32_e32 v4, 0x42800000, v5
	v_mul_f32_e32 v5, 0x42800000, v9
	v_mov_b32_e32 v8, v3
	v_cvt_pk_fp8_f32 v8, v4, v5
	s_lshl_b32 s14, s14, 8
	v_mul_f32_e32 v4, 0x42800000, v13
	v_mul_f32_e32 v5, 0x42800000, v17
	s_sub_i32 s7, s7, s14
	v_cvt_pk_fp8_f32 v8, v4, v5 op_sel:[0,0,1]
	v_mul_f32_e32 v4, 0x42800000, v6
	v_mul_f32_e32 v5, 0x42800000, v10
	v_mov_b32_e32 v10, v3
	s_sext_i32_i16 s14, s7
	v_cvt_pk_fp8_f32 v10, v4, v5
	v_mul_f32_e32 v4, 0x42800000, v7
	v_mul_f32_e32 v5, 0x42800000, v11
	v_mov_b32_e32 v7, v3
	s_bfe_u32 s14, s14, 0x4001b
	v_mul_f32_e32 v12, 0x42800000, v12
	v_mul_f32_e32 v16, 0x42800000, v16
	v_cvt_pk_fp8_f32 v7, v4, v5
	s_add_i32 s7, s7, s14
	v_cvt_pk_fp8_f32 v20, v12, v16 op_sel:[0,0,1]
	s_sext_i32_i16 s7, s7
	v_mul_f32_e32 v22, 0x42800000, v30
	v_mul_f32_e32 v24, 0x42800000, v34
	v_mul_f32_e32 v6, 0x42800000, v14
	v_mul_f32_e32 v9, 0x42800000, v18
	v_cvt_pk_fp8_f32 v26, v22, v24 op_sel:[0,0,1]
	v_cvt_pk_fp8_f32 v10, v6, v9 op_sel:[0,0,1]
	v_mul_f32_e32 v4, 0x42800000, v15
	v_mul_f32_e32 v5, 0x42800000, v19
	s_lshl_b32 s7, s7, 3
	v_cvt_pk_fp8_f32 v7, v4, v5 op_sel:[0,0,1]
	v_lshlrev_b32_e32 v1, 4, v1
	s_and_b32 s7, s7, 0xffffff80
	ds_write2_b32 v2, v101, v20 offset1:16
	ds_write2_b32 v2, v25, v8 offset0:36 offset1:52
	ds_write2_b32 v2, v26, v10 offset0:72 offset1:88
	ds_write2_b32 v2, v23, v7 offset0:108 offset1:124
	v_and_b32_e32 v2, 0x70, v1
	s_ashr_i32 s14, s7, 31
	v_mul_lo_u32 v1, v100, s91
	s_add_u32 s16, s16, s7
	v_add3_u32 v1, 0, v2, v1
	s_waitcnt lgkmcnt(0)
	s_barrier
	s_addc_u32 s17, s17, s14
	ds_read_b128 v[4:7], v1
	v_ashrrev_i32_e32 v101, 31, v100
	v_lshl_add_u64 v[8:9], s[16:17], 0, v[2:3]
	v_lshlrev_b64 v[10:11], 11, v[100:101]
	v_lshl_add_u64 v[12:13], v[8:9], 0, v[10:11]
	ds_read_b128 v[8:11], v1 offset:9216
	s_waitcnt lgkmcnt(1)
	global_store_dwordx4 v[12:13], v[4:7], off
	s_add_i32 s4, s4, 1
	s_add_i32 s5, s5, 32
	v_add_co_u32_e32 v4, vcc, 0x20000, v12
	v_mov_b64_e32 v[20:21], v[80:81]
	s_nop 0
	v_addc_co_u32_e32 v5, vcc, 0, v13, vcc
	s_waitcnt lgkmcnt(0)
	global_store_dwordx4 v[4:5], v[8:11], off
	v_mov_b64_e32 v[24:25], v[68:69]
	v_mov_b64_e32 v[28:29], v[64:65]
	v_mov_b64_e32 v[32:33], v[60:61]
	v_mov_b64_e32 v[4:5], v[56:57]
	v_mov_b64_e32 v[8:9], v[52:53]
	v_mov_b64_e32 v[12:13], v[48:49]
	v_mov_b64_e32 v[16:17], v[44:45]
	s_cmpk_eq_i32 s4, 0x4e
	v_mov_b64_e32 v[22:23], v[82:83]
	v_mov_b64_e32 v[26:27], v[70:71]
	v_mov_b64_e32 v[30:31], v[66:67]
	v_mov_b64_e32 v[34:35], v[62:63]
	v_mov_b64_e32 v[6:7], v[58:59]
	v_mov_b64_e32 v[10:11], v[54:55]
	v_mov_b64_e32 v[14:15], v[50:51]
	v_mov_b64_e32 v[18:19], v[46:47]
	s_barrier
	s_cbranch_scc1 .LBB0_783
; DEVI int opaque_tid() { int t = threadIdx.x; asm volatile("" : "+v"(t)); return t; }
; DEVI void cvt8_load(const Params& p, int L, int t, CvtIn& in) {
;     const int which = t / 4096, r = t % 4096, le = L * 16 + r / 256, kt = (r % 256) / 16, nt = r % 16;
;     const float* src = (which == 2 ? p.w_down : (which == 0 ? p.w_gate : p.w_up)) + (size_t)le * 2048 * 2048;
;     const int tid = opaque_tid(), nq = tid & 31, kq0 = tid >> 5;
; #pragma unroll
;     for (int it = 0; it < 2; ++it)
; #pragma unroll
;         for (int kk = 0; kk < 4; ++kk) in.v[it * 4 + kk] = __builtin_nontemporal_load((const f32x4*)(src + (size_t)(kt * 128 + (kq0 + it * 16) * 4 + kk) * 2048 + nt * 128 + nq * 4));
; }
; DEVI void cvt8_stream3(const Params& p, int L, int t0, int step, int count, char* smem) {
;     ...
;     for (int i = 0; i < count; ++i) { CvtIn c;
;         if (i + 2 < count) cvt8_load(p, L, t0 + (i + 2) * step, c);
.LBB0_777:
	s_waitcnt vmcnt(0)
	v_mov_b64_e32 v[44:45], v[96:97]
	v_mov_b64_e32 v[48:49], v[92:93]
	v_mov_b64_e32 v[52:53], v[88:89]
	v_mov_b64_e32 v[56:57], v[84:85]
	v_mov_b64_e32 v[60:61], v[76:77]
	v_mov_b64_e32 v[64:65], v[72:73]
	v_mov_b64_e32 v[70:71], v[42:43]
	v_mov_b64_e32 v[82:83], v[38:39]
	v_mov_b64_e32 v[46:47], v[98:99]
	v_mov_b64_e32 v[50:51], v[94:95]
	v_mov_b64_e32 v[54:55], v[90:91]
	v_mov_b64_e32 v[58:59], v[86:87]
	v_mov_b64_e32 v[62:63], v[78:79]
	v_mov_b64_e32 v[66:67], v[74:75]
	v_mov_b64_e32 v[68:69], v[40:41]
	s_cmpk_gt_u32 s4, 0x4b
	v_mov_b64_e32 v[80:81], v[36:37]
	s_cbranch_scc1 .LBB0_779
	s_add_i32 s7, s5, 0xfffff001
	s_and_b32 s14, s7, 0xfffff000
	s_cmpk_lt_u32 s5, 0x1fff
	s_cselect_b32 s16, s64, 0x80
	s_cmpk_lg_i32 s14, 0x2000
	s_cselect_b32 s14, s16, 0x88
	s_add_u32 s16, s0, s14
	s_addc_u32 s17, s1, 0
	s_ashr_i32 s14, s7, 31
	s_lshr_b32 s14, s14, 20
	s_add_i32 s14, s7, s14
	s_and_b32 s14, s14, 0xf000
	s_sub_i32 s7, s7, s14
	s_sext_i32_i16 s14, s7
	s_lshr_b32 s14, s14, 15
	s_bfe_u32 s18, s14, 0x4000c
	s_add_i32 s18, s7, s18
	s_and_b32 s18, s18, 0xfff0
	s_bfe_u32 s14, s14, 0x80008
	s_sub_i32 s18, s7, s18
	s_add_i32 s14, s7, s14
	s_sext_i32_i16 s23, s18
	s_sext_i32_i16 s18, s14
	s_and_b32 s14, s14, 0xff00
	s_load_dwordx2 s[16:17], s[16:17], 0x0
	s_ashr_i32 s18, s18, 8
	s_sub_i32 s7, s7, s14
	s_sext_i32_i16 s14, s7
	s_add_i32 s18, s18, 16
	s_bfe_u32 s14, s14, 0x4001b
	s_and_b32 s52, s18, 0xffff
	s_add_i32 s7, s7, s14
	s_lshl_b64 s[18:19], s[52:53], 24
	s_waitcnt lgkmcnt(0)
	s_add_u32 s14, s16, s18
	s_sext_i32_i16 s7, s7
	s_addc_u32 s18, s17, s19
	v_mov_b32_e32 v1, v0
	s_lshl_b32 s16, s23, 7
	s_lshl_b32 s7, s7, 3
	v_ashrrev_i32_e32 v2, 3, v1
	s_ashr_i32 s17, s16, 31
	s_and_b32 s7, s7, 0xffffff80
	v_and_b32_e32 v2, -4, v2
	s_lshl_b64 s[16:17], s[16:17], 2
	v_add_u32_e32 v72, s7, v2
	s_add_u32 s16, s14, s16
	v_lshlrev_b32_e32 v1, 4, v1
	s_addc_u32 s17, s18, s17
	v_and_b32_e32 v2, 0x1f0, v1
	v_ashrrev_i32_e32 v73, 31, v72
	v_lshl_add_u64 v[74:75], s[16:17], 0, v[2:3]
	v_lshlrev_b64 v[36:37], 13, v[72:73]
	v_lshl_add_u64 v[92:93], v[74:75], 0, v[36:37]
	v_add_co_u32_e32 v84, vcc, s94, v92
	v_or_b32_e32 v36, 1, v72
	s_nop 0
	v_addc_co_u32_e32 v85, vcc, 0, v93, vcc
	v_add_co_u32_e32 v88, vcc, 0x82000, v92
	v_or_b32_e32 v76, 2, v72
	s_nop 0
	v_addc_co_u32_e32 v89, vcc, 0, v93, vcc
	v_or_b32_e32 v72, 3, v72
	v_add_co_u32_e32 v94, vcc, 0x84000, v92
	v_ashrrev_i32_e32 v37, 31, v36
	v_ashrrev_i32_e32 v77, 31, v76
	v_ashrrev_i32_e32 v73, 31, v72
	v_addc_co_u32_e32 v95, vcc, 0, v93, vcc
	v_lshlrev_b64 v[36:37], 13, v[36:37]
	v_lshlrev_b64 v[76:77], 13, v[76:77]
	v_lshlrev_b64 v[72:73], 13, v[72:73]
	v_add_co_u32_e32 v96, vcc, 0x86000, v92
	v_lshl_add_u64 v[40:41], v[74:75], 0, v[36:37]
	v_lshl_add_u64 v[76:77], v[74:75], 0, v[76:77]
	v_lshl_add_u64 v[78:79], v[74:75], 0, v[72:73]
	v_addc_co_u32_e32 v97, vcc, 0, v93, vcc
	global_load_dwordx4 v[36:39], v[92:93], off nt
	s_nop 0
	global_load_dwordx4 v[40:43], v[40:41], off nt
	s_nop 0
	global_load_dwordx4 v[72:75], v[76:77], off nt
	s_nop 0
	global_load_dwordx4 v[76:79], v[78:79], off nt
	s_nop 0
	global_load_dwordx4 v[84:87], v[84:85], off nt
	s_nop 0
	global_load_dwordx4 v[88:91], v[88:89], off nt
	s_nop 0
	global_load_dwordx4 v[92:95], v[94:95], off nt
	s_nop 0
	global_load_dwordx4 v[96:99], v[96:97], off nt

; DEVI int opaque_tid() { int t = threadIdx.x; asm volatile("" : "+v"(t)); return t; }
; DEVI void cvt8_load(const Params& p, int L, int t, CvtIn& in) {
;     const int which = t / 4096, r = t % 4096, le = L * 16 + r / 256, kt = (r % 256) / 16, nt = r % 16;
;     const float* src = (which == 2 ? p.w_down : (which == 0 ? p.w_gate : p.w_up)) + (size_t)le * 2048 * 2048;
;     const int tid = opaque_tid(), nq = tid & 31, kq0 = tid >> 5;
; #pragma unroll
;     for (int it = 0; it < 2; ++it)
; #pragma unroll
;         for (int kk = 0; kk < 4; ++kk) in.v[it * 4 + kk] = __builtin_nontemporal_load((const f32x4*)(src + (size_t)(kt * 128 + (kq0 + it * 16) * 4 + kk) * 2048 + nt * 128 + nq * 4));
; }
; DEVI void cvt8_stream3(const Params& p, int L, int t0, int step, int count, char* smem) {
;     if (count <= 0) return;
;     CvtIn a, b; cvt8_load(p, L, t0, a);
;     if (count > 1) cvt8_load(p, L, t0 + step, b);
.LBB0_784:
	s_and_b64 vcc, exec, s[16:17]
	s_cbranch_vccz .LBB0_801
	s_add_i32 s7, s6, 0x1fd0
	s_and_b32 s4, s7, 0xfffff000
	s_add_i32 s5, s6, 0x2fcf
	s_cmpk_lt_u32 s5, 0x1fff
	s_cselect_b32 s5, s64, 0x80
	s_cmpk_lg_i32 s4, 0x2000
	s_cselect_b32 s4, s5, 0x88
	s_add_u32 s4, s0, s4
	s_addc_u32 s5, s1, 0
	s_ashr_i32 s14, s7, 31
	s_lshr_b32 s14, s14, 20
	s_add_i32 s14, s7, s14
	s_and_b32 s14, s14, 0xf000
	s_sub_i32 s7, s7, s14
	s_sext_i32_i16 s14, s7
	s_lshr_b32 s14, s14, 15
	s_bfe_u32 s16, s14, 0x4000c
	s_add_i32 s16, s7, s16
	s_and_b32 s16, s16, 0xfff0
	s_sub_i32 s16, s7, s16
	s_bfe_u32 s14, s14, 0x80008
	s_sext_i32_i16 s18, s16
	s_add_i32 s16, s7, s14
	s_sext_i32_i16 s14, s16
	s_and_b32 s16, s16, 0xff00
	s_sub_i32 s7, s7, s16
	s_load_dwordx2 s[4:5], s[4:5], 0x0
	s_sext_i32_i16 s16, s7
	s_lshr_b32 s14, s14, 8
	s_bfe_u32 s16, s16, 0x4001b
	s_add_i32 s7, s7, s16
	s_bfe_i64 s[16:17], s[14:15], 0x100000
	s_lshl_b64 s[16:17], s[16:17], 24
	s_sext_i32_i16 s7, s7
	s_waitcnt lgkmcnt(0)
	s_add_u32 s14, s4, s16
	v_mov_b32_e32 v1, v0
	s_addc_u32 s16, s5, s17
	s_lshl_b32 s4, s7, 3
	v_ashrrev_i32_e32 v2, 3, v1
	s_and_b32 s4, s4, 0xffffff80
	v_and_b32_e32 v2, -4, v2
	s_waitcnt vmcnt(2)
	v_add_u32_e32 v4, s4, v2
	s_lshl_b32 s4, s18, 7
	s_ashr_i32 s5, s4, 31
	s_lshl_b64 s[4:5], s[4:5], 2
	s_add_u32 s4, s14, s4
	v_lshlrev_b32_e32 v1, 4, v1
	s_addc_u32 s5, s16, s5
	v_and_b32_e32 v2, 0x1f0, v1
	v_ashrrev_i32_e32 v5, 31, v4
	v_lshl_add_u64 v[6:7], s[4:5], 0, v[2:3]
	s_waitcnt vmcnt(1)
	v_lshlrev_b64 v[8:9], 13, v[4:5]
	v_lshl_add_u64 v[12:13], v[6:7], 0, v[8:9]
	v_or_b32_e32 v8, 1, v4
	v_ashrrev_i32_e32 v9, 31, v8
	v_lshlrev_b64 v[8:9], 13, v[8:9]
	v_lshl_add_u64 v[8:9], v[6:7], 0, v[8:9]
	global_load_dwordx4 v[20:23], v[12:13], off nt
	global_load_dwordx4 v[24:27], v[8:9], off nt
	v_or_b32_e32 v8, 2, v4
	v_or_b32_e32 v4, 3, v4
	v_ashrrev_i32_e32 v9, 31, v8
	v_ashrrev_i32_e32 v5, 31, v4
	v_lshlrev_b64 v[8:9], 13, v[8:9]
	v_lshlrev_b64 v[4:5], 13, v[4:5]
	v_lshl_add_u64 v[8:9], v[6:7], 0, v[8:9]
	v_lshl_add_u64 v[4:5], v[6:7], 0, v[4:5]
	global_load_dwordx4 v[28:31], v[8:9], off nt
	global_load_dwordx4 v[32:35], v[4:5], off nt
	v_add_co_u32_e32 v4, vcc, s94, v12
	s_mov_b32 s19, 0x82000
	s_nop 0
	v_addc_co_u32_e32 v5, vcc, 0, v13, vcc
	v_add_co_u32_e32 v8, vcc, s19, v12
	s_mov_b32 s4, 0x84000
	s_nop 0
	v_addc_co_u32_e32 v9, vcc, 0, v13, vcc
	v_add_co_u32_e32 v14, vcc, s4, v12
	s_mov_b32 s4, 0x86000
	s_nop 0
	v_addc_co_u32_e32 v15, vcc, 0, v13, vcc
	s_add_i32 s7, s6, 0x1ff0
	v_add_co_u32_e32 v16, vcc, s4, v12
	s_and_b32 s4, s7, 0xfffff000
	s_add_i32 s5, s6, 0x2fef
	s_cmpk_lt_u32 s5, 0x1fff
	s_cselect_b32 s5, s64, 0x80
	s_cmpk_lg_i32 s4, 0x2000
	s_cselect_b32 s4, s5, 0x88
	s_add_u32 s4, s0, s4
	s_addc_u32 s5, s1, 0
	s_ashr_i32 s14, s7, 31
	s_lshr_b32 s14, s14, 20
	s_add_i32 s14, s7, s14
	s_and_b32 s14, s14, 0xf000
	s_sub_i32 s7, s7, s14
	s_sext_i32_i16 s14, s7
	s_lshr_b32 s14, s14, 15
	s_bfe_u32 s16, s14, 0x4000c
	s_add_i32 s16, s7, s16
	s_and_b32 s16, s16, 0xfff0
	s_sub_i32 s16, s7, s16
	s_bfe_u32 s14, s14, 0x80008
	s_sext_i32_i16 s18, s16
	s_add_i32 s16, s7, s14
	v_addc_co_u32_e32 v17, vcc, 0, v13, vcc
	s_sext_i32_i16 s14, s16
	s_and_b32 s16, s16, 0xff00
	global_load_dwordx4 v[4:7], v[4:5], off nt
	s_nop 0
	global_load_dwordx4 v[8:11], v[8:9], off nt
	s_nop 0
	global_load_dwordx4 v[12:15], v[14:15], off nt
	s_nop 0
	global_load_dwordx4 v[16:19], v[16:17], off nt
	s_sub_i32 s7, s7, s16
	s_load_dwordx2 s[4:5], s[4:5], 0x0
	s_sext_i32_i16 s16, s7
	s_lshr_b32 s14, s14, 8
	s_bfe_u32 s16, s16, 0x4001b
	s_add_i32 s7, s7, s16
	s_bfe_i64 s[16:17], s[14:15], 0x100000
	s_lshl_b64 s[16:17], s[16:17], 24
	s_sext_i32_i16 s7, s7
	s_waitcnt lgkmcnt(0)
	s_add_u32 s14, s4, s16
	v_mov_b32_e32 v1, v0
	s_addc_u32 s16, s5, s17
	s_lshl_b32 s4, s7, 3
	v_ashrrev_i32_e32 v2, 3, v1
	s_and_b32 s4, s4, 0xffffff80
	v_and_b32_e32 v2, -4, v2
	v_add_u32_e32 v44, s4, v2
	s_lshl_b32 s4, s18, 7
	s_ashr_i32 s5, s4, 31
	s_lshl_b64 s[4:5], s[4:5], 2
	s_add_u32 s4, s14, s4
	v_lshlrev_b32_e32 v1, 4, v1
	s_addc_u32 s5, s16, s5
	v_and_b32_e32 v2, 0x1f0, v1
	v_ashrrev_i32_e32 v45, 31, v44
	v_lshl_add_u64 v[46:47], s[4:5], 0, v[2:3]
	v_lshlrev_b64 v[36:37], 13, v[44:45]
	v_lshl_add_u64 v[48:49], v[46:47], 0, v[36:37]
	v_or_b32_e32 v36, 1, v44
	v_or_b32_e32 v50, 2, v44
	v_or_b32_e32 v44, 3, v44
	v_ashrrev_i32_e32 v37, 31, v36
	v_ashrrev_i32_e32 v51, 31, v50
	v_ashrrev_i32_e32 v45, 31, v44
	v_lshlrev_b64 v[36:37], 13, v[36:37]
	v_lshlrev_b64 v[50:51], 13, v[50:51]
	v_lshlrev_b64 v[44:45], 13, v[44:45]
	v_lshl_add_u64 v[40:41], v[46:47], 0, v[36:37]
	v_lshl_add_u64 v[50:51], v[46:47], 0, v[50:51]
	v_lshl_add_u64 v[44:45], v[46:47], 0, v[44:45]
	global_load_dwordx4 v[36:39], v[48:49], off nt
	s_nop 0
	global_load_dwordx4 v[40:43], v[40:41], off nt
	s_nop 0
	global_load_dwordx4 v[72:75], v[50:51], off nt
	global_load_dwordx4 v[76:79], v[44:45], off nt
	v_add_co_u32_e32 v44, vcc, s94, v48
	s_mov_b32 s4, 0
	s_nop 0
	v_addc_co_u32_e32 v45, vcc, 0, v49, vcc
	v_add_co_u32_e32 v46, vcc, s19, v48
	s_add_i32 s5, s6, 0x300f
	s_nop 0
	v_addc_co_u32_e32 v47, vcc, 0, v49, vcc
	global_load_dwordx4 v[84:87], v[44:45], off nt
	global_load_dwordx4 v[88:91], v[46:47], off nt
	v_add_co_u32_e32 v44, vcc, 0x84000, v48
	s_nop 1
	v_addc_co_u32_e32 v45, vcc, 0, v49, vcc
	v_add_co_u32_e32 v46, vcc, 0x86000, v48
	s_nop 1
	v_addc_co_u32_e32 v47, vcc, 0, v49, vcc
	global_load_dwordx4 v[92:95], v[44:45], off nt
	global_load_dwordx4 v[96:99], v[46:47], off nt
	s_branch .LBB0_787
; DEVI int opaque_tid() { int t = threadIdx.x; asm volatile("" : "+v"(t)); return t; }
; DEVI unsigned cvt4_fp8(float a, float b, float c, float d) { int w = 0; w = __builtin_amdgcn_cvt_pk_fp8_f32(a, b, w, false); w = __builtin_amdgcn_cvt_pk_fp8_f32(c, d, w, true); return (unsigned)w; }
; DEVI void cvt8_finish(const Params& p, int L, int t, const CvtIn& in, char* smem) {
;     const int which = t / 4096, r = t % 4096, le = L * 16 + r / 256, kt = (r % 256) / 16, nt = r % 16;
;     unsigned char* dst = (which == 2) ? (unsigned char*)(p.ws + WS_WDN) + (size_t)le * 2048 * 2048 + (size_t)(nt * 128) * 2048
;                                       : (unsigned char*)(p.ws + WS_WGU) + (size_t)le * 4096 * 2048 + (size_t)(nt * 256 + which * 128) * 2048;
;     unsigned char* T = (unsigned char*)smem;
;     const int tid = opaque_tid(), nq = tid & 31, kq0 = tid >> 5;
; #pragma unroll
;     for (int it = 0; it < 2; ++it) { const int kq = kq0 + it * 16;
; #pragma unroll
;         for (int j = 0; j < 4; ++j) *(unsigned*)(T + (nq * 4 + j) * 144 + kq * 4) =
;             cvt4_fp8(in.v[it * 4][j] * W8_SCALE, in.v[it * 4 + 1][j] * W8_SCALE, in.v[it * 4 + 2][j] * W8_SCALE, in.v[it * 4 + 3][j] * W8_SCALE); }
;     __syncthreads();
; #pragma unroll
;     for (int i = 0; i < 2; ++i) { const int nl = (tid >> 3) + 64 * i, kc = (tid & 7) * 16;
;         *(u32x4*)(dst + (size_t)nl * 2048 + kt * 128 + kc) = *(const u32x4*)(T + nl * 144 + kc); }
;     __syncthreads();
; }
; DEVI void cvt8_stream3(const Params& p, int L, int t0, int step, int count, char* smem) {
;     ...
;     for (int i = 0; i < count; ++i) { CvtIn c;
;         if (i + 2 < count) cvt8_load(p, L, t0 + (i + 2) * step, c);
;         cvt8_finish(p, L, t0 + i * step, a, smem);
;         a = b; b = c; }
.LBB0_786:
	v_mul_f32_e32 v20, 0x42800000, v20
	v_mul_f32_e32 v24, 0x42800000, v24
	v_mov_b32_e32 v101, v3
	v_cvt_pk_fp8_f32 v101, v20, v24
	v_mul_f32_e32 v24, 0x42800000, v28
	v_mul_f32_e32 v28, 0x42800000, v32
	v_mov_b32_e32 v1, v0
	v_cvt_pk_fp8_f32 v101, v24, v28 op_sel:[0,0,1]
	v_mul_f32_e32 v21, 0x42800000, v21
	v_mul_f32_e32 v24, 0x42800000, v25
	v_mov_b32_e32 v25, v3
	v_cvt_pk_fp8_f32 v25, v21, v24
	v_lshlrev_b32_e32 v2, 2, v1
	v_and_b32_e32 v2, 0x7c, v2
	v_ashrrev_i32_e32 v100, 3, v1
	v_and_b32_e32 v20, -4, v100
	v_mul_u32_u24_e32 v2, 0x90, v2
	v_add3_u32 v2, 0, v20, v2
	v_mul_f32_e32 v20, 0x42800000, v29
	v_mul_f32_e32 v21, 0x42800000, v33
	v_cvt_pk_fp8_f32 v25, v20, v21 op_sel:[0,0,1]
	v_mul_f32_e32 v20, 0x42800000, v22
	v_mul_f32_e32 v21, 0x42800000, v26
	v_mov_b32_e32 v26, v3
	v_cvt_pk_fp8_f32 v26, v20, v21
	v_mul_f32_e32 v20, 0x42800000, v23
	v_mul_f32_e32 v21, 0x42800000, v27
	v_mov_b32_e32 v23, v3
	v_cvt_pk_fp8_f32 v23, v20, v21
	v_mul_f32_e32 v20, 0x42800000, v31
	v_mul_f32_e32 v21, 0x42800000, v35
	v_mul_f32_e32 v4, 0x42800000, v4
	v_cvt_pk_fp8_f32 v23, v20, v21 op_sel:[0,0,1]
	v_mul_f32_e32 v8, 0x42800000, v8
	v_mov_b32_e32 v20, v3
	v_cvt_pk_fp8_f32 v20, v4, v8
	v_mul_f32_e32 v4, 0x42800000, v5
	v_mul_f32_e32 v5, 0x42800000, v9
	v_mov_b32_e32 v8, v3
	v_cvt_pk_fp8_f32 v8, v4, v5
	s_lshl_b32 s14, s14, 8
	v_mul_f32_e32 v4, 0x42800000, v13
	v_mul_f32_e32 v5, 0x42800000, v17
	s_sub_i32 s7, s7, s14
	v_cvt_pk_fp8_f32 v8, v4, v5 op_sel:[0,0,1]
	v_mul_f32_e32 v4, 0x42800000, v6
	v_mul_f32_e32 v5, 0x42800000, v10
	v_mov_b32_e32 v10, v3
	s_sext_i32_i16 s14, s7
	v_cvt_pk_fp8_f32 v10, v4, v5
	v_mul_f32_e32 v4, 0x42800000, v7
	v_mul_f32_e32 v5, 0x42800000, v11
	v_mov_b32_e32 v7, v3
	s_bfe_u32 s14, s14, 0x4001b
	v_mul_f32_e32 v12, 0x42800000, v12
	v_mul_f32_e32 v16, 0x42800000, v16
	v_cvt_pk_fp8_f32 v7, v4, v5
	s_add_i32 s7, s7, s14
	v_cvt_pk_fp8_f32 v20, v12, v16 op_sel:[0,0,1]
	s_sext_i32_i16 s7, s7
	v_mul_f32_e32 v22, 0x42800000, v30
	v_mul_f32_e32 v24, 0x42800000, v34
	v_mul_f32_e32 v6, 0x42800000, v14
	v_mul_f32_e32 v9, 0x42800000, v18
	v_cvt_pk_fp8_f32 v26, v22, v24 op_sel:[0,0,1]
	v_cvt_pk_fp8_f32 v10, v6, v9 op_sel:[0,0,1]
	v_mul_f32_e32 v4, 0x42800000, v15
	v_mul_f32_e32 v5, 0x42800000, v19
	s_lshl_b32 s7, s7, 3
	v_cvt_pk_fp8_f32 v7, v4, v5 op_sel:[0,0,1]
	v_lshlrev_b32_e32 v1, 4, v1
	s_and_b32 s7, s7, 0xffffff80
	ds_write2_b32 v2, v101, v20 offset1:16
	ds_write2_b32 v2, v25, v8 offset0:36 offset1:52
	ds_write2_b32 v2, v26, v10 offset0:72 offset1:88
	ds_write2_b32 v2, v23, v7 offset0:108 offset1:124
	v_and_b32_e32 v2, 0x70, v1
	s_ashr_i32 s14, s7, 31
	v_mul_lo_u32 v1, v100, s91
	s_add_u32 s16, s16, s7
	v_add3_u32 v1, 0, v2, v1
	s_waitcnt lgkmcnt(0)
	s_barrier
	s_addc_u32 s17, s17, s14
	ds_read_b128 v[4:7], v1
	v_ashrrev_i32_e32 v101, 31, v100
	v_lshl_add_u64 v[8:9], s[16:17], 0, v[2:3]
	v_lshlrev_b64 v[10:11], 11, v[100:101]
	v_lshl_add_u64 v[12:13], v[8:9], 0, v[10:11]
	ds_read_b128 v[8:11], v1 offset:9216
	s_waitcnt lgkmcnt(1)
	global_store_dwordx4 v[12:13], v[4:7], off
	s_add_i32 s4, s4, 1
	s_add_i32 s5, s5, 32
	v_add_co_u32_e32 v4, vcc, 0x20000, v12
	v_mov_b64_e32 v[20:21], v[80:81]
	s_nop 0
	v_addc_co_u32_e32 v5, vcc, 0, v13, vcc
	s_waitcnt lgkmcnt(0)
	global_store_dwordx4 v[4:5], v[8:11], off
	v_mov_b64_e32 v[24:25], v[68:69]
	v_mov_b64_e32 v[28:29], v[64:65]
	v_mov_b64_e32 v[32:33], v[60:61]
	v_mov_b64_e32 v[4:5], v[56:57]
	v_mov_b64_e32 v[8:9], v[52:53]
	v_mov_b64_e32 v[12:13], v[48:49]
	v_mov_b64_e32 v[16:17], v[44:45]
	s_cmp_lg_u32 s4, 50
	v_mov_b64_e32 v[22:23], v[82:83]
	v_mov_b64_e32 v[26:27], v[70:71]
	v_mov_b64_e32 v[30:31], v[66:67]
	v_mov_b64_e32 v[34:35], v[62:63]
	v_mov_b64_e32 v[6:7], v[58:59]
	v_mov_b64_e32 v[10:11], v[54:55]
	v_mov_b64_e32 v[14:15], v[50:51]
	v_mov_b64_e32 v[18:19], v[46:47]
	s_barrier
	s_cbranch_scc0 .LBB0_793
; DEVI int opaque_tid() { int t = threadIdx.x; asm volatile("" : "+v"(t)); return t; }
; DEVI void cvt8_load(const Params& p, int L, int t, CvtIn& in) {
;     const int which = t / 4096, r = t % 4096, le = L * 16 + r / 256, kt = (r % 256) / 16, nt = r % 16;
;     const float* src = (which == 2 ? p.w_down : (which == 0 ? p.w_gate : p.w_up)) + (size_t)le * 2048 * 2048;
;     const int tid = opaque_tid(), nq = tid & 31, kq0 = tid >> 5;
; #pragma unroll
;     for (int it = 0; it < 2; ++it)
; #pragma unroll
;         for (int kk = 0; kk < 4; ++kk) in.v[it * 4 + kk] = __builtin_nontemporal_load((const f32x4*)(src + (size_t)(kt * 128 + (kq0 + it * 16) * 4 + kk) * 2048 + nt * 128 + nq * 4));
; }
; DEVI void cvt8_stream3(const Params& p, int L, int t0, int step, int count, char* smem) {
;     ...
;     for (int i = 0; i < count; ++i) { CvtIn c;
;         if (i + 2 < count) cvt8_load(p, L, t0 + (i + 2) * step, c);
.LBB0_787:
	s_waitcnt vmcnt(0)
	v_mov_b64_e32 v[44:45], v[96:97]
	v_mov_b64_e32 v[48:49], v[92:93]
	v_mov_b64_e32 v[52:53], v[88:89]
	v_mov_b64_e32 v[56:57], v[84:85]
	v_mov_b64_e32 v[60:61], v[76:77]
	v_mov_b64_e32 v[64:65], v[72:73]
	v_mov_b64_e32 v[70:71], v[42:43]
	v_mov_b64_e32 v[82:83], v[38:39]
	v_mov_b64_e32 v[46:47], v[98:99]
	v_mov_b64_e32 v[50:51], v[94:95]
	v_mov_b64_e32 v[54:55], v[90:91]
	v_mov_b64_e32 v[58:59], v[86:87]
	v_mov_b64_e32 v[62:63], v[78:79]
	v_mov_b64_e32 v[66:67], v[74:75]
	v_mov_b64_e32 v[68:69], v[40:41]
	s_cmp_gt_u32 s4, 47
	v_mov_b64_e32 v[80:81], v[36:37]
	s_cbranch_scc1 .LBB0_789
	s_add_i32 s7, s5, 0xfffff001
	s_and_b32 s14, s7, 0xfffff000
	s_cmpk_lt_u32 s5, 0x1fff
	s_cselect_b32 s16, s64, 0x80
	s_cmpk_lg_i32 s14, 0x2000
	s_cselect_b32 s14, s16, 0x88
	s_add_u32 s16, s0, s14
	s_addc_u32 s17, s1, 0
	s_ashr_i32 s14, s7, 31
	s_lshr_b32 s14, s14, 20
	s_add_i32 s14, s7, s14
	s_and_b32 s14, s14, 0xf000
	s_sub_i32 s7, s7, s14
	s_sext_i32_i16 s14, s7
	s_lshr_b32 s14, s14, 15
	s_bfe_u32 s18, s14, 0x4000c
	s_add_i32 s18, s7, s18
	s_and_b32 s18, s18, 0xfff0
	s_sub_i32 s18, s7, s18
	s_bfe_u32 s14, s14, 0x80008
	s_sext_i32_i16 s23, s18
	s_add_i32 s18, s7, s14
	s_sext_i32_i16 s14, s18
	s_and_b32 s18, s18, 0xff00
	s_sub_i32 s7, s7, s18
	s_load_dwordx2 s[16:17], s[16:17], 0x0
	s_sext_i32_i16 s18, s7
	s_lshr_b32 s14, s14, 8
	s_bfe_u32 s18, s18, 0x4001b
	s_add_i32 s7, s7, s18
	s_bfe_i64 s[18:19], s[14:15], 0x100000
	s_lshl_b64 s[18:19], s[18:19], 24
	s_waitcnt lgkmcnt(0)
	s_add_u32 s14, s16, s18
	s_sext_i32_i16 s7, s7
	s_addc_u32 s18, s17, s19
	v_mov_b32_e32 v1, v0
	s_lshl_b32 s16, s23, 7
	s_lshl_b32 s7, s7, 3
	v_ashrrev_i32_e32 v2, 3, v1
	s_ashr_i32 s17, s16, 31
	s_and_b32 s7, s7, 0xffffff80
	v_and_b32_e32 v2, -4, v2
	s_lshl_b64 s[16:17], s[16:17], 2
	v_add_u32_e32 v72, s7, v2
	s_add_u32 s16, s14, s16
	v_lshlrev_b32_e32 v1, 4, v1
	s_addc_u32 s17, s18, s17
	v_and_b32_e32 v2, 0x1f0, v1
	v_ashrrev_i32_e32 v73, 31, v72
	v_lshl_add_u64 v[74:75], s[16:17], 0, v[2:3]
	v_lshlrev_b64 v[36:37], 13, v[72:73]
	v_lshl_add_u64 v[92:93], v[74:75], 0, v[36:37]
	v_add_co_u32_e32 v84, vcc, s94, v92
	v_or_b32_e32 v36, 1, v72
	s_nop 0
	v_addc_co_u32_e32 v85, vcc, 0, v93, vcc
	v_add_co_u32_e32 v88, vcc, 0x82000, v92
	v_or_b32_e32 v76, 2, v72
	s_nop 0
	v_addc_co_u32_e32 v89, vcc, 0, v93, vcc
	v_or_b32_e32 v72, 3, v72
	v_add_co_u32_e32 v94, vcc, 0x84000, v92
	v_ashrrev_i32_e32 v37, 31, v36
	v_ashrrev_i32_e32 v77, 31, v76
	v_ashrrev_i32_e32 v73, 31, v72
	v_addc_co_u32_e32 v95, vcc, 0, v93, vcc
	v_lshlrev_b64 v[36:37], 13, v[36:37]
	v_lshlrev_b64 v[76:77], 13, v[76:77]
	v_lshlrev_b64 v[72:73], 13, v[72:73]
	v_add_co_u32_e32 v96, vcc, 0x86000, v92
	v_lshl_add_u64 v[40:41], v[74:75], 0, v[36:37]
	v_lshl_add_u64 v[76:77], v[74:75], 0, v[76:77]
	v_lshl_add_u64 v[78:79], v[74:75], 0, v[72:73]
	v_addc_co_u32_e32 v97, vcc, 0, v93, vcc
	global_load_dwordx4 v[36:39], v[92:93], off nt
	s_nop 0
	global_load_dwordx4 v[40:43], v[40:41], off nt
	s_nop 0
	global_load_dwordx4 v[72:75], v[76:77], off nt
	s_nop 0
	global_load_dwordx4 v[76:79], v[78:79], off nt
	s_nop 0
	global_load_dwordx4 v[84:87], v[84:85], off nt
	s_nop 0
	global_load_dwordx4 v[88:91], v[88:89], off nt
	s_nop 0
	global_load_dwordx4 v[92:95], v[94:95], off nt
	s_nop 0
	global_load_dwordx4 v[96:99], v[96:97], off nt

; DEVI int opaque_tid() { int t = threadIdx.x; asm volatile("" : "+v"(t)); return t; }
; DEVI void cvt8_load(const Params& p, int L, int t, CvtIn& in) {
;     const int which = t / 4096, r = t % 4096, le = L * 16 + r / 256, kt = (r % 256) / 16, nt = r % 16;
;     const float* src = (which == 2 ? p.w_down : (which == 0 ? p.w_gate : p.w_up)) + (size_t)le * 2048 * 2048;
;     const int tid = opaque_tid(), nq = tid & 31, kq0 = tid >> 5;
; #pragma unroll
;     for (int it = 0; it < 2; ++it)
; #pragma unroll
;         for (int kk = 0; kk < 4; ++kk) in.v[it * 4 + kk] = __builtin_nontemporal_load((const f32x4*)(src + (size_t)(kt * 128 + (kq0 + it * 16) * 4 + kk) * 2048 + nt * 128 + nq * 4));
; }
; DEVI void cvt8_stream3(const Params& p, int L, int t0, int step, int count, char* smem) {
;     if (count <= 0) return;
;     CvtIn a, b; cvt8_load(p, L, t0, a);
;     if (count > 1) cvt8_load(p, L, t0 + step, b);
.LBB0_793:
	s_add_i32 s7, s6, 0x1890
	s_and_b32 s4, s7, 0xfffff000
	s_add_i32 s5, s6, 0x288f
	s_cmpk_lt_u32 s5, 0x1fff
	s_cselect_b32 s5, s64, 0x80
	s_cmpk_lg_i32 s4, 0x2000
	s_cselect_b32 s4, s5, 0x88
	s_add_u32 s4, s0, s4
	s_addc_u32 s5, s1, 0
	s_ashr_i32 s14, s7, 31
	s_lshr_b32 s14, s14, 20
	s_add_i32 s14, s7, s14
	s_and_b32 s14, s14, 0xf000
	s_sub_i32 s7, s7, s14
	s_sext_i32_i16 s14, s7
	s_lshr_b32 s14, s14, 15
	s_bfe_u32 s16, s14, 0x4000c
	s_add_i32 s16, s7, s16
	s_and_b32 s16, s16, 0xfff0
	s_bfe_u32 s14, s14, 0x80008
	s_sub_i32 s16, s7, s16
	s_add_i32 s14, s7, s14
	s_sext_i32_i16 s18, s16
	s_sext_i32_i16 s16, s14
	s_and_b32 s14, s14, 0xff00
	s_load_dwordx2 s[4:5], s[4:5], 0x0
	s_ashr_i32 s16, s16, 8
	s_sub_i32 s7, s7, s14
	s_sext_i32_i16 s14, s7
	s_add_i32 s16, s16, 16
	s_bfe_u32 s14, s14, 0x4001b
	s_and_b32 s52, s16, 0xffff
	s_add_i32 s7, s7, s14
	s_lshl_b64 s[16:17], s[52:53], 24
	s_sext_i32_i16 s7, s7
	s_waitcnt lgkmcnt(0)
	s_add_u32 s14, s4, s16
	v_mov_b32_e32 v1, v0
	s_addc_u32 s16, s5, s17
	s_lshl_b32 s4, s7, 3
	v_ashrrev_i32_e32 v2, 3, v1
	s_and_b32 s4, s4, 0xffffff80
	v_and_b32_e32 v2, -4, v2
	v_add_u32_e32 v4, s4, v2
	s_lshl_b32 s4, s18, 7
	s_ashr_i32 s5, s4, 31
	s_lshl_b64 s[4:5], s[4:5], 2
	s_add_u32 s4, s14, s4
	v_lshlrev_b32_e32 v1, 4, v1
	s_addc_u32 s5, s16, s5
	v_and_b32_e32 v2, 0x1f0, v1
	v_ashrrev_i32_e32 v5, 31, v4
	v_lshl_add_u64 v[6:7], s[4:5], 0, v[2:3]
	v_lshlrev_b64 v[8:9], 13, v[4:5]
	v_lshl_add_u64 v[12:13], v[6:7], 0, v[8:9]
	v_or_b32_e32 v8, 1, v4
	v_ashrrev_i32_e32 v9, 31, v8
	v_lshlrev_b64 v[8:9], 13, v[8:9]
	v_lshl_add_u64 v[8:9], v[6:7], 0, v[8:9]
	global_load_dwordx4 v[20:23], v[12:13], off nt
	global_load_dwordx4 v[24:27], v[8:9], off nt
	v_or_b32_e32 v8, 2, v4
	v_or_b32_e32 v4, 3, v4
	v_ashrrev_i32_e32 v9, 31, v8
	v_ashrrev_i32_e32 v5, 31, v4
	v_lshlrev_b64 v[8:9], 13, v[8:9]
	v_lshlrev_b64 v[4:5], 13, v[4:5]
	v_lshl_add_u64 v[8:9], v[6:7], 0, v[8:9]
	v_lshl_add_u64 v[4:5], v[6:7], 0, v[4:5]
	global_load_dwordx4 v[28:31], v[8:9], off nt
	global_load_dwordx4 v[32:35], v[4:5], off nt
	v_add_co_u32_e32 v4, vcc, s94, v12
	s_mov_b32 s4, 0x82000
	s_nop 0
	v_addc_co_u32_e32 v5, vcc, 0, v13, vcc
	v_add_co_u32_e32 v8, vcc, s4, v12
	s_mov_b32 s4, 0x84000
	s_nop 0
	v_addc_co_u32_e32 v9, vcc, 0, v13, vcc
	v_add_co_u32_e32 v14, vcc, s4, v12
	s_mov_b32 s4, 0x86000
	s_nop 0
	v_addc_co_u32_e32 v15, vcc, 0, v13, vcc
	s_add_i32 s7, s6, 0x18b0
	v_add_co_u32_e32 v16, vcc, s4, v12
	s_and_b32 s4, s7, 0xfffff000
	s_add_i32 s5, s6, 0x28af
	s_cmpk_lt_u32 s5, 0x1fff
	s_cselect_b32 s5, s64, 0x80
	s_cmpk_lg_i32 s4, 0x2000
	s_cselect_b32 s4, s5, 0x88
	s_add_u32 s4, s0, s4
	s_addc_u32 s5, s1, 0
	s_ashr_i32 s14, s7, 31
	s_lshr_b32 s14, s14, 20
	s_add_i32 s14, s7, s14
	s_and_b32 s14, s14, 0xf000
	s_sub_i32 s7, s7, s14
	s_sext_i32_i16 s14, s7
	s_lshr_b32 s14, s14, 15
	s_bfe_u32 s16, s14, 0x4000c
	s_add_i32 s16, s7, s16
	s_and_b32 s16, s16, 0xfff0
	s_bfe_u32 s14, s14, 0x80008
	v_addc_co_u32_e32 v17, vcc, 0, v13, vcc
	s_sub_i32 s16, s7, s16
	s_add_i32 s14, s7, s14
	global_load_dwordx4 v[4:7], v[4:5], off nt
	s_nop 0
	global_load_dwordx4 v[8:11], v[8:9], off nt
	s_nop 0
	global_load_dwordx4 v[12:15], v[14:15], off nt
	s_nop 0
	global_load_dwordx4 v[16:19], v[16:17], off nt
	s_sext_i32_i16 s18, s16
	s_sext_i32_i16 s16, s14
	s_and_b32 s14, s14, 0xff00
	s_load_dwordx2 s[4:5], s[4:5], 0x0
	s_ashr_i32 s16, s16, 8
	s_sub_i32 s7, s7, s14
	s_sext_i32_i16 s14, s7
	s_add_i32 s16, s16, 16
	s_bfe_u32 s14, s14, 0x4001b
	s_and_b32 s52, s16, 0xffff
	s_add_i32 s7, s7, s14
	s_lshl_b64 s[16:17], s[52:53], 24
	s_sext_i32_i16 s7, s7
	s_waitcnt lgkmcnt(0)
	s_add_u32 s14, s4, s16
	v_mov_b32_e32 v1, v0
	s_addc_u32 s16, s5, s17
	s_lshl_b32 s4, s7, 3
	v_ashrrev_i32_e32 v2, 3, v1
	s_and_b32 s4, s4, 0xffffff80
	v_and_b32_e32 v2, -4, v2
	v_add_u32_e32 v44, s4, v2
	s_lshl_b32 s4, s18, 7
	s_ashr_i32 s5, s4, 31
	s_lshl_b64 s[4:5], s[4:5], 2
	s_add_u32 s4, s14, s4
	v_lshlrev_b32_e32 v1, 4, v1
	s_addc_u32 s5, s16, s5
	v_and_b32_e32 v2, 0x1f0, v1
	v_ashrrev_i32_e32 v45, 31, v44
	v_lshl_add_u64 v[46:47], s[4:5], 0, v[2:3]
	s_waitcnt vmcnt(17)
	v_lshlrev_b64 v[36:37], 13, v[44:45]
	v_lshl_add_u64 v[48:49], v[46:47], 0, v[36:37]
	v_or_b32_e32 v36, 1, v44
	v_or_b32_e32 v50, 2, v44
	v_or_b32_e32 v44, 3, v44
	v_ashrrev_i32_e32 v37, 31, v36
	v_ashrrev_i32_e32 v51, 31, v50
	v_ashrrev_i32_e32 v45, 31, v44
	v_lshlrev_b64 v[36:37], 13, v[36:37]
	v_lshlrev_b64 v[50:51], 13, v[50:51]
	v_lshlrev_b64 v[44:45], 13, v[44:45]
	s_waitcnt vmcnt(16)
	v_lshl_add_u64 v[40:41], v[46:47], 0, v[36:37]
	v_lshl_add_u64 v[50:51], v[46:47], 0, v[50:51]
	v_lshl_add_u64 v[44:45], v[46:47], 0, v[44:45]
	global_load_dwordx4 v[36:39], v[48:49], off nt
	s_nop 0
	global_load_dwordx4 v[40:43], v[40:41], off nt
	s_nop 0
	global_load_dwordx4 v[72:75], v[50:51], off nt
	global_load_dwordx4 v[76:79], v[44:45], off nt
	v_add_co_u32_e32 v44, vcc, s94, v48
	s_mov_b32 s4, 0
	s_nop 0
	v_addc_co_u32_e32 v45, vcc, 0, v49, vcc
	v_add_co_u32_e32 v46, vcc, 0x82000, v48
	s_add_i32 s5, s6, 0x28cf
	s_nop 0
	v_addc_co_u32_e32 v47, vcc, 0, v49, vcc
	global_load_dwordx4 v[84:87], v[44:45], off nt
	global_load_dwordx4 v[88:91], v[46:47], off nt
	v_add_co_u32_e32 v44, vcc, 0x84000, v48
	s_nop 1
	v_addc_co_u32_e32 v45, vcc, 0, v49, vcc
	v_add_co_u32_e32 v46, vcc, 0x86000, v48
	s_nop 1
	v_addc_co_u32_e32 v47, vcc, 0, v49, vcc
	global_load_dwordx4 v[92:95], v[44:45], off nt
	global_load_dwordx4 v[96:99], v[46:47], off nt
	s_branch .LBB0_795

; DEVI int obid() { int b = blockIdx.x; asm volatile("" : "+s"(b)); return b; }
; DEVI int opaque_tid() { int t = threadIdx.x; asm volatile("" : "+v"(t)); return t; }
; DEVI unsigned cvt4_fp8(float a, float b, float c, float d) { int w = 0; w = __builtin_amdgcn_cvt_pk_fp8_f32(a, b, w, false); w = __builtin_amdgcn_cvt_pk_fp8_f32(c, d, w, true); return (unsigned)w; }
; DEVI void cvt8_finish(const Params& p, int L, int t, const CvtIn& in, char* smem) {
;     const int which = t / 4096, r = t % 4096, le = L * 16 + r / 256, kt = (r % 256) / 16, nt = r % 16;
;     unsigned char* dst = (which == 2) ? (unsigned char*)(p.ws + WS_WDN) + (size_t)le * 2048 * 2048 + (size_t)(nt * 128) * 2048
;                                       : (unsigned char*)(p.ws + WS_WGU) + (size_t)le * 4096 * 2048 + (size_t)(nt * 256 + which * 128) * 2048;
;     unsigned char* T = (unsigned char*)smem;
;     const int tid = opaque_tid(), nq = tid & 31, kq0 = tid >> 5;
; #pragma unroll
;     for (int it = 0; it < 2; ++it) { const int kq = kq0 + it * 16;
; #pragma unroll
;         for (int j = 0; j < 4; ++j) *(unsigned*)(T + (nq * 4 + j) * 144 + kq * 4) =
;             cvt4_fp8(in.v[it * 4][j] * W8_SCALE, in.v[it * 4 + 1][j] * W8_SCALE, in.v[it * 4 + 2][j] * W8_SCALE, in.v[it * 4 + 3][j] * W8_SCALE); }
;     __syncthreads();
; #pragma unroll
;     for (int i = 0; i < 2; ++i) { const int nl = (tid >> 3) + 64 * i, kc = (tid & 7) * 16;
;         *(u32x4*)(dst + (size_t)nl * 2048 + kt * 128 + kc) = *(const u32x4*)(T + nl * 144 + kc); }
;     __syncthreads();
; }
; DEVI void phase_rank(const Params& p, int l, char* smem) {
;     ...
;     if (gridDim.x == 256) {
;         const int first = 64, bid = obid();
;         const int nt = (l == 0) ? RANKT0 : RANKT1;
;         if (bid >= first) cvt8_stream3(p, l, ((l == 0) ? T0B : T1B) + (bid - first), 256 - first, nt, smem);
;     }
.LBB0_1167:
	v_mul_f32_e32 v12, 0x42800000, v12
	v_mul_f32_e32 v16, 0x42800000, v16
	v_mov_b32_e32 v101, v3
	v_cvt_pk_fp8_f32 v101, v12, v16
	v_mul_f32_e32 v16, 0x42800000, v20
	v_mul_f32_e32 v20, 0x42800000, v24
	v_mov_b32_e32 v1, v0
	v_cvt_pk_fp8_f32 v101, v16, v20 op_sel:[0,0,1]
	v_mul_f32_e32 v13, 0x42800000, v13
	v_mul_f32_e32 v16, 0x42800000, v17
	v_mov_b32_e32 v17, v3
	v_cvt_pk_fp8_f32 v17, v13, v16
	v_lshlrev_b32_e32 v2, 2, v1
	v_and_b32_e32 v2, 0x7c, v2
	v_ashrrev_i32_e32 v100, 3, v1
	v_and_b32_e32 v12, -4, v100
	v_mul_u32_u24_e32 v2, 0x90, v2
	v_add3_u32 v2, 0, v12, v2
	v_mul_f32_e32 v12, 0x42800000, v21
	v_mul_f32_e32 v13, 0x42800000, v25
	v_cvt_pk_fp8_f32 v17, v12, v13 op_sel:[0,0,1]
	v_mul_f32_e32 v12, 0x42800000, v14
	v_mul_f32_e32 v13, 0x42800000, v18
	v_mov_b32_e32 v18, v3
	v_cvt_pk_fp8_f32 v18, v12, v13
	v_mul_f32_e32 v14, 0x42800000, v22
	v_mul_f32_e32 v16, 0x42800000, v26
	v_mul_f32_e32 v4, 0x42800000, v4
	v_cvt_pk_fp8_f32 v18, v14, v16 op_sel:[0,0,1]
	v_mul_f32_e32 v8, 0x42800000, v8
	v_mov_b32_e32 v14, v3
	v_cvt_pk_fp8_f32 v14, v4, v8
	v_mul_f32_e32 v4, 0x42800000, v5
	v_mul_f32_e32 v5, 0x42800000, v9
	v_mov_b32_e32 v8, v3
	v_cvt_pk_fp8_f32 v8, v4, v5
	v_mul_f32_e32 v12, 0x42800000, v15
	v_mul_f32_e32 v13, 0x42800000, v19
	v_mov_b32_e32 v15, v3
	s_lshr_b32 s15, s15, 8
	v_cvt_pk_fp8_f32 v15, v12, v13
	s_lshl_b32 s15, s15, 8
	v_mul_f32_e32 v4, 0x42800000, v29
	v_mul_f32_e32 v5, 0x42800000, v33
	s_sub_i32 s14, s14, s15
	v_cvt_pk_fp8_f32 v8, v4, v5 op_sel:[0,0,1]
	v_mul_f32_e32 v4, 0x42800000, v6
	v_mul_f32_e32 v5, 0x42800000, v10
	v_mov_b32_e32 v10, v3
	s_sext_i32_i16 s15, s14
	v_mul_f32_e32 v12, 0x42800000, v23
	v_mul_f32_e32 v13, 0x42800000, v27
	v_cvt_pk_fp8_f32 v10, v4, v5
	v_mul_f32_e32 v4, 0x42800000, v7
	v_mul_f32_e32 v5, 0x42800000, v11
	v_mov_b32_e32 v7, v3
	s_bfe_u32 s15, s15, 0x4001b
	v_cvt_pk_fp8_f32 v15, v12, v13 op_sel:[0,0,1]
	v_mul_f32_e32 v12, 0x42800000, v28
	v_mul_f32_e32 v13, 0x42800000, v32
	v_cvt_pk_fp8_f32 v7, v4, v5
	s_add_i32 s14, s14, s15
	v_cvt_pk_fp8_f32 v14, v12, v13 op_sel:[0,0,1]
	s_sext_i32_i16 s14, s14
	v_mul_f32_e32 v6, 0x42800000, v30
	v_mul_f32_e32 v9, 0x42800000, v34
	v_cvt_pk_fp8_f32 v10, v6, v9 op_sel:[0,0,1]
	v_mul_f32_e32 v4, 0x42800000, v31
	v_mul_f32_e32 v5, 0x42800000, v35
	s_lshl_b32 s14, s14, 3
	v_cvt_pk_fp8_f32 v7, v4, v5 op_sel:[0,0,1]
	v_lshlrev_b32_e32 v1, 4, v1
	s_and_b32 s14, s14, 0xffffff80
	ds_write2_b32 v2, v101, v14 offset1:16
	ds_write2_b32 v2, v17, v8 offset0:36 offset1:52
	ds_write2_b32 v2, v18, v10 offset0:72 offset1:88
	ds_write2_b32 v2, v15, v7 offset0:108 offset1:124
	v_and_b32_e32 v2, 0x70, v1
	s_ashr_i32 s15, s14, 31
	v_mul_lo_u32 v1, v100, s91
	s_add_u32 s14, s16, s14
	v_add3_u32 v1, 0, v2, v1
	s_waitcnt lgkmcnt(0)
	s_barrier
	s_addc_u32 s15, s17, s15
	ds_read_b128 v[4:7], v1
	v_ashrrev_i32_e32 v101, 31, v100
	v_lshl_add_u64 v[8:9], s[14:15], 0, v[2:3]
	v_lshlrev_b64 v[10:11], 11, v[100:101]
	v_lshl_add_u64 v[12:13], v[8:9], 0, v[10:11]
	ds_read_b128 v[8:11], v1 offset:9216
	s_waitcnt lgkmcnt(1)
	global_store_dwordx4 v[12:13], v[4:7], off
	s_add_i32 s7, s7, 1
	s_addk_i32 s4, 0xc0
	v_add_co_u32_e32 v4, vcc, 0x20000, v12
	v_mov_b64_e32 v[16:17], v[68:69]
	s_nop 0
	v_addc_co_u32_e32 v5, vcc, 0, v13, vcc
	s_waitcnt lgkmcnt(0)
	global_store_dwordx4 v[4:5], v[8:11], off
	v_mov_b64_e32 v[12:13], v[80:81]
	v_mov_b64_e32 v[20:21], v[64:65]
	v_mov_b64_e32 v[24:25], v[60:61]
	v_mov_b64_e32 v[4:5], v[56:57]
	v_mov_b64_e32 v[8:9], v[52:53]
	v_mov_b64_e32 v[28:29], v[48:49]
	v_mov_b64_e32 v[32:33], v[44:45]
	s_cmp_lg_u32 s7, 16
	v_mov_b64_e32 v[14:15], v[82:83]
	v_mov_b64_e32 v[18:19], v[70:71]
	v_mov_b64_e32 v[22:23], v[66:67]
	v_mov_b64_e32 v[26:27], v[62:63]
	v_mov_b64_e32 v[6:7], v[58:59]
	v_mov_b64_e32 v[10:11], v[54:55]
	v_mov_b64_e32 v[30:31], v[50:51]
	v_mov_b64_e32 v[34:35], v[46:47]
	s_barrier
	s_cbranch_scc0 .LBB0_1174
; DEVI int opaque_tid() { int t = threadIdx.x; asm volatile("" : "+v"(t)); return t; }
; DEVI void cvt8_load(const Params& p, int L, int t, CvtIn& in) {
;     const int which = t / 4096, r = t % 4096, le = L * 16 + r / 256, kt = (r % 256) / 16, nt = r % 16;
;     const float* src = (which == 2 ? p.w_down : (which == 0 ? p.w_gate : p.w_up)) + (size_t)le * 2048 * 2048;
;     const int tid = opaque_tid(), nq = tid & 31, kq0 = tid >> 5;
; #pragma unroll
;     for (int it = 0; it < 2; ++it)
; #pragma unroll
;         for (int kk = 0; kk < 4; ++kk) in.v[it * 4 + kk] = __builtin_nontemporal_load((const f32x4*)(src + (size_t)(kt * 128 + (kq0 + it * 16) * 4 + kk) * 2048 + nt * 128 + nq * 4));
; }
; DEVI void cvt8_stream3(const Params& p, int L, int t0, int step, int count, char* smem) {
;     ...
;     for (int i = 0; i < count; ++i) { CvtIn c;
;         if (i + 2 < count) cvt8_load(p, L, t0 + (i + 2) * step, c);
.LBB0_1168:
	s_waitcnt vmcnt(0)
	v_mov_b64_e32 v[44:45], v[96:97]
	v_mov_b64_e32 v[48:49], v[92:93]
	v_mov_b64_e32 v[52:53], v[88:89]
	v_mov_b64_e32 v[56:57], v[84:85]
	v_mov_b64_e32 v[60:61], v[76:77]
	v_mov_b64_e32 v[64:65], v[72:73]
	v_mov_b64_e32 v[70:71], v[42:43]
	v_mov_b64_e32 v[82:83], v[38:39]
	v_mov_b64_e32 v[46:47], v[98:99]
	v_mov_b64_e32 v[50:51], v[94:95]
	v_mov_b64_e32 v[54:55], v[90:91]
	v_mov_b64_e32 v[58:59], v[86:87]
	v_mov_b64_e32 v[62:63], v[78:79]
	v_mov_b64_e32 v[66:67], v[74:75]
	v_mov_b64_e32 v[68:69], v[40:41]
	s_cmp_gt_u32 s7, 13
	v_mov_b64_e32 v[80:81], v[36:37]
	s_cbranch_scc1 .LBB0_1170
	s_add_i32 s16, s4, 0x180
	s_and_b32 s14, s16, 0xfffff000
	s_cmpk_lt_u32 s16, 0x1000
	s_cselect_b32 s15, s64, 0x80
	s_cmpk_lg_i32 s14, 0x2000
	s_cselect_b32 s14, s15, 0x88
	s_add_u32 s14, s0, s14
	s_addc_u32 s15, s1, 0
	s_ashr_i32 s17, s16, 31
	s_lshr_b32 s17, s17, 20
	s_add_i32 s17, s16, s17
	s_and_b32 s17, s17, 0xf000
	s_sub_i32 s16, s16, s17
	s_sext_i32_i16 s17, s16
	s_lshr_b32 s17, s17, 15
	s_bfe_u32 s18, s17, 0x4000c
	s_bfe_u32 s17, s17, 0x80008
	s_add_i32 s18, s16, s18
	s_add_i32 s17, s16, s17
	s_and_b32 s18, s18, 0xfff0
	s_sext_i32_i16 s19, s17
	s_and_b32 s17, s17, 0xff00
	s_sub_i32 s18, s16, s18
	s_sub_i32 s16, s16, s17
	s_sext_i32_i16 s17, s16
	s_bfe_u32 s17, s17, 0x4001b
	s_add_i32 s16, s16, s17
	s_load_dwordx2 s[14:15], s[14:15], 0x0
	s_sext_i32_i16 s23, s16
	s_ashr_i32 s16, s19, 8
	s_add_i32 s16, s5, s16
	s_ashr_i32 s17, s16, 31
	s_lshl_b64 s[16:17], s[16:17], 24
	s_waitcnt lgkmcnt(0)
	s_add_u32 s16, s14, s16
	v_mov_b32_e32 v1, v0
	s_addc_u32 s17, s15, s17
	s_lshl_b32 s14, s23, 3
	v_ashrrev_i32_e32 v2, 3, v1
	s_sext_i32_i16 s18, s18
	s_and_b32 s14, s14, 0xffffff80
	v_and_b32_e32 v2, -4, v2
	v_add_u32_e32 v72, s14, v2
	s_lshl_b32 s14, s18, 7
	s_ashr_i32 s15, s14, 31
	s_lshl_b64 s[14:15], s[14:15], 2
	s_add_u32 s14, s16, s14
	v_lshlrev_b32_e32 v1, 4, v1
	s_addc_u32 s15, s17, s15
	v_and_b32_e32 v2, 0x1f0, v1
	v_ashrrev_i32_e32 v73, 31, v72
	v_lshl_add_u64 v[74:75], s[14:15], 0, v[2:3]
	v_lshlrev_b64 v[36:37], 13, v[72:73]
	v_lshl_add_u64 v[92:93], v[74:75], 0, v[36:37]
	v_add_co_u32_e32 v84, vcc, s94, v92
	v_or_b32_e32 v36, 1, v72
	s_nop 0
	v_addc_co_u32_e32 v85, vcc, 0, v93, vcc
	v_add_co_u32_e32 v88, vcc, 0x82000, v92
	v_or_b32_e32 v76, 2, v72
	s_nop 0
	v_addc_co_u32_e32 v89, vcc, 0, v93, vcc
	v_or_b32_e32 v72, 3, v72
	v_add_co_u32_e32 v94, vcc, 0x84000, v92
	v_ashrrev_i32_e32 v37, 31, v36
	v_ashrrev_i32_e32 v77, 31, v76
	v_ashrrev_i32_e32 v73, 31, v72
	v_addc_co_u32_e32 v95, vcc, 0, v93, vcc
	v_lshlrev_b64 v[36:37], 13, v[36:37]
	v_lshlrev_b64 v[76:77], 13, v[76:77]
	v_lshlrev_b64 v[72:73], 13, v[72:73]
	v_add_co_u32_e32 v96, vcc, 0x86000, v92
	v_lshl_add_u64 v[40:41], v[74:75], 0, v[36:37]
	v_lshl_add_u64 v[76:77], v[74:75], 0, v[76:77]
	v_lshl_add_u64 v[78:79], v[74:75], 0, v[72:73]
	v_addc_co_u32_e32 v97, vcc, 0, v93, vcc
	global_load_dwordx4 v[36:39], v[92:93], off nt
	s_nop 0
	global_load_dwordx4 v[40:43], v[40:41], off nt
	s_nop 0
	global_load_dwordx4 v[72:75], v[76:77], off nt
	s_nop 0
	global_load_dwordx4 v[76:79], v[78:79], off nt
	s_nop 0
	global_load_dwordx4 v[84:87], v[84:85], off nt
	s_nop 0
	global_load_dwordx4 v[88:91], v[88:89], off nt
	s_nop 0
	global_load_dwordx4 v[92:95], v[94:95], off nt
	s_nop 0
	global_load_dwordx4 v[96:99], v[96:97], off nt
